# v52 + attention K/V tile address arithmetic hoisted out of the QK-to-PV transition block into QK gaps (m0 computed directly)
# baseline (speedup 1.0000x reference)
.LBB0_336:
	ds_read_b64_tr_b16 v[144:145], v211 offset:49152
	ds_read_b64_tr_b16 v[146:147], v211 offset:49664
	s_waitcnt lgkmcnt(9)
	v_mfma_f32_32x32x16_bf16 v[84:99], v[68:71], v[140:143], -4.0
	v_pk_add_f16 v0, v72, v150
	v_pk_add_f16 v68, v73, v151
	v_cvt_pk_f16_f32 v124, v52, v53
	v_pk_add_f16 v0, v0, v68
	v_cvt_pk_f16_f32 v125, v54, v55
	v_dot2c_f32_f16_e32 v2, 0x3c003c00, v0
	ds_read_b64_tr_b16 v[52:53], v211 offset:53248
	ds_read_b64_tr_b16 v[54:55], v211 offset:53760
	s_waitcnt lgkmcnt(10)
	v_mfma_f32_32x32x16_bf16 v[68:83], v[160:163], v[140:143], -4.0
	s_add_u32 s56, s88, s54
	s_addc_u32 s57, s89, s55
	s_add_u32 s58, s14, s54
	s_addc_u32 s59, s15, s55
	v_exp_f32_e32 v44, v44
	v_cvt_pk_f16_f32 v126, v56, v57
	v_cvt_pk_f16_f32 v127, v58, v59
	ds_read_b64_tr_b16 v[56:57], v211 offset:50176
	ds_read_b64_tr_b16 v[58:59], v211 offset:50688
	s_waitcnt lgkmcnt(11)
	v_mfma_f32_32x32x16_bf16 v[84:99], v[156:159], v[128:131], v[84:99]
	v_exp_f32_e32 v45, v45
	v_pk_add_f16 v0, v124, v126
	v_pk_add_f16 v116, v125, v127
	v_cvt_pk_f16_f32 v120, v60, v61
	v_cvt_pk_f16_f32 v121, v62, v63
	ds_read_b64_tr_b16 v[60:61], v211 offset:54272
	ds_read_b64_tr_b16 v[62:63], v211 offset:54784
	s_waitcnt lgkmcnt(12)
	v_mfma_f32_32x32x16_bf16 v[68:83], v[112:115], v[128:131], v[68:83]
	v_exp_f32_e32 v46, v46
	v_exp_f32_e32 v47, v47
	v_pk_add_f16 v0, v0, v120
	v_pk_add_f16 v116, v116, v121
	v_cvt_pk_f16_f32 v122, v64, v65
	v_cvt_pk_f16_f32 v123, v66, v67
	ds_read_b64_tr_b16 v[64:65], v211 offset:51200
	ds_read_b64_tr_b16 v[66:67], v211 offset:51712
	s_waitcnt lgkmcnt(13)
	v_mfma_f32_32x32x16_bf16 v[84:99], v[152:155], v[136:139], v[84:99]
	v_exp_f32_e32 v48, v48
	v_exp_f32_e32 v49, v49
	v_pk_add_f16 v0, v0, v122
	v_pk_add_f16 v112, v116, v123
	v_cvt_pk_f16_f32 v116, v36, v37
	v_cvt_pk_f16_f32 v117, v38, v39
	ds_read_b64_tr_b16 v[36:37], v211 offset:55296
	ds_read_b64_tr_b16 v[38:39], v211 offset:55808
	s_waitcnt lgkmcnt(14)
	v_mfma_f32_32x32x16_bf16 v[68:83], v[104:107], v[136:139], v[68:83]
	v_exp_f32_e32 v50, v50
	v_pk_add_f16 v0, v0, v116
	v_pk_add_f16 v112, v112, v117
	v_cvt_pk_f16_f32 v118, v40, v41
	v_cvt_pk_f16_f32 v119, v42, v43
	ds_read_b64_tr_b16 v[40:41], v211 offset:52224
	ds_read_b64_tr_b16 v[42:43], v211 offset:52736
	v_cvt_pk_f16_f32 v148, v44, v45
	v_pk_add_f16 v0, v0, v118
	v_pk_add_f16 v104, v112, v119
	v_cvt_pk_f16_f32 v149, v46, v47
	s_waitcnt lgkmcnt(14)
	v_mfma_f32_32x32x16_bf16 v[84:99], v[108:111], v[132:135], v[84:99]
	s_add_u32 s60, s56, 0x48000
	s_addc_u32 s61, s57, 0
	s_add_u32 s62, s58, 0x30000
	s_addc_u32 s63, s59, 0
	v_exp_f32_e32 v51, v51
	ds_read_b64_tr_b16 v[44:45], v211 offset:56320
	ds_read_b64_tr_b16 v[46:47], v211 offset:56832
	v_mfma_f32_32x32x16_bf16 v[68:83], v[100:103], v[132:135], v[68:83]
	v_pk_add_f16 v0, v0, v148
	v_pk_add_f16 v166, v104, v149
	v_cvt_pk_f16_f32 v150, v48, v49
	v_cvt_pk_f16_f32 v151, v50, v51
	s_mov_b32 m0, s70
	s_nop 0
	global_load_lds_dwordx4 v165, s[60:61]
	s_add_i32 m0, s44, 0x14000
	s_nop 0
	global_load_lds_dwordx4 v164, s[62:63]
	s_waitcnt lgkmcnt(14)
	v_mfma_f32_32x32x16_f16 v[4:19], v[124:127], v[144:147], v[4:19]
	v_exp_f32_e32 v84, v84
	v_exp_f32_e32 v85, v85
	v_exp_f32_e32 v86, v86
	s_waitcnt lgkmcnt(12)
	v_mfma_f32_32x32x16_f16 v[20:35], v[124:127], v[52:55], v[20:35]
	v_exp_f32_e32 v87, v87
	v_exp_f32_e32 v88, v88
	v_exp_f32_e32 v89, v89
	ds_read_b128 v[48:51], v210 offset:16384
	ds_read_b128 v[52:55], v210 offset:16896
	s_waitcnt lgkmcnt(12)
	v_mfma_f32_32x32x16_f16 v[4:19], v[120:123], v[56:59], v[4:19]
	v_exp_f32_e32 v90, v90
	v_exp_f32_e32 v91, v91
	v_exp_f32_e32 v92, v92
	ds_read_b128 v[56:59], v210 offset:18432
	ds_read_b128 v[144:147], v210 offset:18944
	s_waitcnt lgkmcnt(12)
	v_mfma_f32_32x32x16_f16 v[20:35], v[120:123], v[60:63], v[20:35]
	v_exp_f32_e32 v93, v93
	v_exp_f32_e32 v94, v94
	v_exp_f32_e32 v95, v95
	ds_read_b128 v[60:63], v210 offset:20480
	ds_read_b128 v[152:155], v210 offset:20992
	s_waitcnt lgkmcnt(12)
	v_mfma_f32_32x32x16_f16 v[4:19], v[116:119], v[64:67], v[4:19]
	v_exp_f32_e32 v96, v96
	v_exp_f32_e32 v97, v97
	v_exp_f32_e32 v98, v98
	ds_read_b128 v[64:67], v210 offset:22528
	ds_read_b128 v[156:159], v210 offset:23040
	s_waitcnt lgkmcnt(12)
	v_mfma_f32_32x32x16_f16 v[20:35], v[116:119], v[36:39], v[20:35]
	v_exp_f32_e32 v99, v99
	v_exp_f32_e32 v68, v68
	v_exp_f32_e32 v69, v69
	s_waitcnt lgkmcnt(10)
	v_mfma_f32_32x32x16_f16 v[4:19], v[148:151], v[40:43], v[4:19]
	v_exp_f32_e32 v70, v70
	v_exp_f32_e32 v71, v71
	v_exp_f32_e32 v72, v72
	s_waitcnt lgkmcnt(8)
	v_mfma_f32_32x32x16_f16 v[20:35], v[148:151], v[44:47], v[20:35]
	v_exp_f32_e32 v73, v73
	v_exp_f32_e32 v74, v74
	v_exp_f32_e32 v75, v75
	ds_read_b64_tr_b16 v[160:161], v211 offset:57344
	ds_read_b64_tr_b16 v[162:163], v211 offset:57856
	s_waitcnt lgkmcnt(9)
	v_mfma_f32_32x32x16_bf16 v[100:115], v[48:51], v[140:143], -4.0
	v_exp_f32_e32 v76, v76
	v_cvt_pk_f16_f32 v124, v84, v85
	v_pk_add_f16 v0, v0, v150
	v_pk_add_f16 v116, v166, v151
	v_cvt_pk_f16_f32 v125, v86, v87
	ds_read_b64_tr_b16 v[84:85], v211 offset:61440
	ds_read_b64_tr_b16 v[86:87], v211 offset:61952
	s_waitcnt lgkmcnt(10)
	v_mfma_f32_32x32x16_bf16 v[36:51], v[52:55], v[140:143], -4.0
	v_exp_f32_e32 v77, v77
	v_pk_add_f16 v0, v0, v124
	v_pk_add_f16 v116, v116, v125
	v_cvt_pk_f16_f32 v126, v88, v89
	v_cvt_pk_f16_f32 v127, v90, v91
	ds_read_b64_tr_b16 v[52:53], v211 offset:58368
	ds_read_b64_tr_b16 v[54:55], v211 offset:58880
	s_waitcnt lgkmcnt(11)
	v_mfma_f32_32x32x16_bf16 v[100:115], v[56:59], v[128:131], v[100:115]
	v_exp_f32_e32 v78, v78
	v_cvt_pk_f16_f32 v120, v92, v93
	v_pk_add_f16 v0, v0, v126
	v_pk_add_f16 v88, v116, v127
	v_cvt_pk_f16_f32 v121, v94, v95
	ds_read_b64_tr_b16 v[56:57], v211 offset:62464
	ds_read_b64_tr_b16 v[58:59], v211 offset:62976
	s_waitcnt lgkmcnt(12)
	v_mfma_f32_32x32x16_bf16 v[36:51], v[144:147], v[128:131], v[36:51]
	v_exp_f32_e32 v79, v79
	v_exp_f32_e32 v80, v80
	v_pk_add_f16 v0, v0, v120
	v_pk_add_f16 v92, v88, v121
	v_cvt_pk_f16_f32 v122, v96, v97
	v_cvt_pk_f16_f32 v123, v98, v99
	ds_read_b64_tr_b16 v[88:89], v211 offset:59392
	ds_read_b64_tr_b16 v[90:91], v211 offset:59904
	s_waitcnt lgkmcnt(13)
	v_mfma_f32_32x32x16_bf16 v[100:115], v[60:63], v[136:139], v[100:115]
	v_exp_f32_e32 v81, v81
	v_cvt_pk_f16_f32 v116, v68, v69
	v_pk_add_f16 v0, v0, v122
	v_pk_add_f16 v92, v92, v123
	v_cvt_pk_f16_f32 v117, v70, v71
	ds_read_b64_tr_b16 v[60:61], v211 offset:63488
	ds_read_b64_tr_b16 v[62:63], v211 offset:64000
	s_waitcnt lgkmcnt(14)
	v_mfma_f32_32x32x16_bf16 v[36:51], v[152:155], v[136:139], v[36:51]
	v_exp_f32_e32 v82, v82
	v_pk_add_f16 v0, v0, v116
	v_pk_add_f16 v92, v92, v117
	v_cvt_pk_f16_f32 v118, v72, v73
	v_cvt_pk_f16_f32 v119, v74, v75
	ds_read_b64_tr_b16 v[68:69], v211 offset:60416
	ds_read_b64_tr_b16 v[70:71], v211 offset:60928
	s_waitcnt lgkmcnt(14)
	v_mfma_f32_32x32x16_bf16 v[100:115], v[64:67], v[132:135], v[100:115]
	s_add_u32 s60, s56, 0x54000
	s_addc_u32 s61, s57, 0
	s_add_u32 s62, s58, 0x3c000
	s_addc_u32 s63, s59, 0
	v_exp_f32_e32 v83, v83
	v_cvt_pk_f16_f32 v148, v76, v77
	v_pk_add_f16 v0, v0, v118
	v_pk_add_f16 v72, v92, v119
	v_cvt_pk_f16_f32 v149, v78, v79
	ds_read_b64_tr_b16 v[64:65], v211 offset:64512
	ds_read_b64_tr_b16 v[66:67], v211 offset:65024
	v_mfma_f32_32x32x16_bf16 v[36:51], v[156:159], v[132:135], v[36:51]
	v_pk_add_f16 v0, v0, v148
	v_pk_add_f16 v170, v72, v149
	v_cvt_pk_f16_f32 v150, v80, v81
	v_cvt_pk_f16_f32 v151, v82, v83
	s_mov_b32 m0, s71
	s_nop 0
	global_load_lds_dwordx4 v165, s[60:61]
	s_add_i32 m0, s44, 0x16000
	s_nop 0
	global_load_lds_dwordx4 v164, s[62:63]
	s_waitcnt lgkmcnt(14)
	v_mfma_f32_32x32x16_f16 v[4:19], v[124:127], v[160:163], v[4:19]
	v_exp_f32_e32 v100, v100
	v_exp_f32_e32 v101, v101
	v_exp_f32_e32 v102, v102
	s_waitcnt lgkmcnt(12)
	v_mfma_f32_32x32x16_f16 v[20:35], v[124:127], v[84:87], v[20:35]
	v_exp_f32_e32 v103, v103
	v_exp_f32_e32 v104, v104
	v_exp_f32_e32 v105, v105
	ds_read_b128 v[92:95], v210 offset:24576
	ds_read_b128 v[96:99], v210 offset:25088
	s_waitcnt lgkmcnt(12)
	v_mfma_f32_32x32x16_f16 v[4:19], v[120:123], v[52:55], v[4:19]
	v_exp_f32_e32 v106, v106
	v_exp_f32_e32 v107, v107
	v_exp_f32_e32 v108, v108
	ds_read_b128 v[144:147], v210 offset:26624
	ds_read_b128 v[152:155], v210 offset:27136
	s_waitcnt lgkmcnt(12)
	v_mfma_f32_32x32x16_f16 v[20:35], v[120:123], v[56:59], v[20:35]
	v_exp_f32_e32 v109, v109
	v_exp_f32_e32 v110, v110
	v_exp_f32_e32 v111, v111
	ds_read_b128 v[156:159], v210 offset:28672
	ds_read_b128 v[160:163], v210 offset:29184
	s_waitcnt lgkmcnt(12)
	v_mfma_f32_32x32x16_f16 v[4:19], v[116:119], v[88:91], v[4:19]
	v_exp_f32_e32 v112, v112
	v_exp_f32_e32 v113, v113
	v_exp_f32_e32 v114, v114
	ds_read_b128 v[88:91], v210 offset:30720
	ds_read_b128 v[84:87], v210 offset:31232
	s_waitcnt lgkmcnt(12)
	v_mfma_f32_32x32x16_f16 v[20:35], v[116:119], v[60:63], v[20:35]
	v_exp_f32_e32 v115, v115
	v_exp_f32_e32 v36, v36
	v_exp_f32_e32 v37, v37
	s_waitcnt lgkmcnt(10)
	v_mfma_f32_32x32x16_f16 v[4:19], v[148:151], v[68:71], v[4:19]
	v_exp_f32_e32 v38, v38
	v_exp_f32_e32 v39, v39
	v_exp_f32_e32 v40, v40
	s_waitcnt lgkmcnt(8)
	v_mfma_f32_32x32x16_f16 v[20:35], v[148:151], v[64:67], v[20:35]
	v_exp_f32_e32 v41, v41
	v_exp_f32_e32 v42, v42
	v_exp_f32_e32 v43, v43
	s_waitcnt vmcnt(4) lgkmcnt(0)
	s_barrier
	ds_read_b64_tr_b16 v[166:167], v212 offset:16384
	ds_read_b64_tr_b16 v[168:169], v212 offset:16896
	s_waitcnt lgkmcnt(9)
	v_mfma_f32_32x32x16_bf16 v[68:83], v[92:95], v[140:143], -4.0
	v_cvt_pk_f16_f32 v124, v100, v101
	v_pk_add_f16 v0, v0, v150
	v_pk_add_f16 v52, v170, v151
	v_pk_add_f16 v0, v0, v52
	v_cvt_pk_f16_f32 v125, v102, v103
	v_dot2c_f32_f16_e32 v2, 0x3c003c00, v0
	ds_read_b64_tr_b16 v[92:93], v212 offset:20480
	ds_read_b64_tr_b16 v[94:95], v212 offset:20992
	s_waitcnt lgkmcnt(10)
	v_mfma_f32_32x32x16_bf16 v[52:67], v[96:99], v[140:143], -4.0
	v_exp_f32_e32 v44, v44
	v_cvt_pk_f16_f32 v126, v104, v105
	v_cvt_pk_f16_f32 v127, v106, v107
	ds_read_b64_tr_b16 v[96:97], v212 offset:17408
	ds_read_b64_tr_b16 v[98:99], v212 offset:17920
	s_waitcnt lgkmcnt(11)
	v_mfma_f32_32x32x16_bf16 v[68:83], v[144:147], v[128:131], v[68:83]
	v_exp_f32_e32 v45, v45
	v_cvt_pk_f16_f32 v120, v108, v109
	v_pk_add_f16 v0, v124, v126
	v_pk_add_f16 v104, v125, v127
	v_cvt_pk_f16_f32 v121, v110, v111
	ds_read_b64_tr_b16 v[100:101], v212 offset:21504
	ds_read_b64_tr_b16 v[102:103], v212 offset:22016
	s_waitcnt lgkmcnt(12)
	v_mfma_f32_32x32x16_bf16 v[52:67], v[152:155], v[128:131], v[52:67]
	v_exp_f32_e32 v46, v46
	v_exp_f32_e32 v47, v47
	v_pk_add_f16 v0, v0, v120
	v_pk_add_f16 v108, v104, v121
	v_cvt_pk_f16_f32 v122, v112, v113
	v_cvt_pk_f16_f32 v123, v114, v115
	ds_read_b64_tr_b16 v[104:105], v212 offset:18432
	ds_read_b64_tr_b16 v[106:107], v212 offset:18944
	s_waitcnt lgkmcnt(13)
	v_mfma_f32_32x32x16_bf16 v[68:83], v[156:159], v[136:139], v[68:83]
	v_exp_f32_e32 v48, v48
	v_exp_f32_e32 v49, v49
	v_cvt_pk_f16_f32 v116, v36, v37
	v_pk_add_f16 v0, v0, v122
	v_pk_add_f16 v108, v108, v123
	v_cvt_pk_f16_f32 v117, v38, v39
	ds_read_b64_tr_b16 v[36:37], v212 offset:22528
	ds_read_b64_tr_b16 v[38:39], v212 offset:23040
	s_waitcnt lgkmcnt(14)
	v_mfma_f32_32x32x16_bf16 v[52:67], v[160:163], v[136:139], v[52:67]
	v_exp_f32_e32 v50, v50
	v_pk_add_f16 v0, v0, v116
	v_pk_add_f16 v108, v108, v117
	v_cvt_pk_f16_f32 v118, v40, v41
	v_cvt_pk_f16_f32 v119, v42, v43
	ds_read_b64_tr_b16 v[40:41], v212 offset:19456
	ds_read_b64_tr_b16 v[42:43], v212 offset:19968
	s_waitcnt lgkmcnt(14)
	v_mfma_f32_32x32x16_bf16 v[68:83], v[88:91], v[132:135], v[68:83]
	s_add_u32 s60, s56, 0x60000
	s_addc_u32 s61, s57, 0
	s_add_u32 s62, s58, 0x48000
	s_addc_u32 s63, s59, 0
	v_exp_f32_e32 v51, v51
	v_cvt_pk_f16_f32 v148, v44, v45
	v_pk_add_f16 v0, v0, v118
	v_pk_add_f16 v88, v108, v119
	v_cvt_pk_f16_f32 v149, v46, v47
	ds_read_b64_tr_b16 v[44:45], v212 offset:23552
	ds_read_b64_tr_b16 v[46:47], v212 offset:24064
	v_mfma_f32_32x32x16_bf16 v[52:67], v[84:87], v[132:135], v[52:67]
	v_pk_add_f16 v0, v0, v148
	v_pk_add_f16 v170, v88, v149
	v_cvt_pk_f16_f32 v150, v48, v49
	v_cvt_pk_f16_f32 v151, v50, v51
	s_mov_b32 m0, s76
	s_nop 0
	global_load_lds_dwordx4 v165, s[60:61]
	s_mov_b32 m0, s10
	s_nop 0
	global_load_lds_dwordx4 v164, s[62:63]
	s_waitcnt lgkmcnt(14)
	v_mfma_f32_32x32x16_f16 v[4:19], v[124:127], v[166:169], v[4:19]
	v_exp_f32_e32 v68, v68
	v_exp_f32_e32 v69, v69
	v_exp_f32_e32 v70, v70
	s_waitcnt lgkmcnt(12)
	v_mfma_f32_32x32x16_f16 v[20:35], v[124:127], v[92:95], v[20:35]
	v_exp_f32_e32 v71, v71
	v_exp_f32_e32 v72, v72
	v_exp_f32_e32 v73, v73
	ds_read_b128 v[48:51], v210 offset:32768
	ds_read_b128 v[84:87], v210 offset:33280
	s_waitcnt lgkmcnt(12)
	v_mfma_f32_32x32x16_f16 v[4:19], v[120:123], v[96:99], v[4:19]
	v_exp_f32_e32 v74, v74
	v_exp_f32_e32 v75, v75
	v_exp_f32_e32 v76, v76
	ds_read_b128 v[88:91], v210 offset:34816
	ds_read_b128 v[92:95], v210 offset:35328
	s_waitcnt lgkmcnt(12)
	v_mfma_f32_32x32x16_f16 v[20:35], v[120:123], v[100:103], v[20:35]
	v_exp_f32_e32 v77, v77
	v_exp_f32_e32 v78, v78
	v_exp_f32_e32 v79, v79
	ds_read_b128 v[96:99], v210 offset:36864
	ds_read_b128 v[144:147], v210 offset:37376
	s_waitcnt lgkmcnt(12)
	v_mfma_f32_32x32x16_f16 v[4:19], v[116:119], v[104:107], v[4:19]
	v_exp_f32_e32 v80, v80
	v_exp_f32_e32 v81, v81
	v_exp_f32_e32 v82, v82
	ds_read_b128 v[152:155], v210 offset:38912
	ds_read_b128 v[156:159], v210 offset:39424
	s_waitcnt lgkmcnt(12)
	v_mfma_f32_32x32x16_f16 v[20:35], v[116:119], v[36:39], v[20:35]
	v_exp_f32_e32 v83, v83
	v_exp_f32_e32 v52, v52
	v_exp_f32_e32 v53, v53
	s_waitcnt lgkmcnt(10)
	v_mfma_f32_32x32x16_f16 v[4:19], v[148:151], v[40:43], v[4:19]
	v_exp_f32_e32 v54, v54
	v_exp_f32_e32 v55, v55
	v_exp_f32_e32 v56, v56
	s_waitcnt lgkmcnt(8)
	v_mfma_f32_32x32x16_f16 v[20:35], v[148:151], v[44:47], v[20:35]
	v_exp_f32_e32 v57, v57
	v_exp_f32_e32 v58, v58
	v_exp_f32_e32 v59, v59
	ds_read_b64_tr_b16 v[160:161], v212 offset:24576
	ds_read_b64_tr_b16 v[162:163], v212 offset:25088
	s_waitcnt lgkmcnt(9)
	v_mfma_f32_32x32x16_bf16 v[100:115], v[48:51], v[140:143], -4.0
	v_exp_f32_e32 v60, v60
	v_cvt_pk_f16_f32 v124, v68, v69
	v_pk_add_f16 v0, v0, v150
	v_pk_add_f16 v116, v170, v151
	v_cvt_pk_f16_f32 v125, v70, v71
	ds_read_b64_tr_b16 v[68:69], v212 offset:28672
	ds_read_b64_tr_b16 v[70:71], v212 offset:29184
	s_waitcnt lgkmcnt(10)
	v_mfma_f32_32x32x16_bf16 v[36:51], v[84:87], v[140:143], -4.0
	v_exp_f32_e32 v61, v61
	v_pk_add_f16 v0, v0, v124
	v_pk_add_f16 v84, v116, v125
	v_cvt_pk_f16_f32 v126, v72, v73
	v_cvt_pk_f16_f32 v127, v74, v75
	ds_read_b64_tr_b16 v[72:73], v212 offset:25600
	ds_read_b64_tr_b16 v[74:75], v212 offset:26112
	s_waitcnt lgkmcnt(11)
	v_mfma_f32_32x32x16_bf16 v[100:115], v[88:91], v[128:131], v[100:115]
	v_exp_f32_e32 v62, v62
	v_cvt_pk_f16_f32 v120, v76, v77
	v_pk_add_f16 v0, v0, v126
	v_pk_add_f16 v84, v84, v127
	v_cvt_pk_f16_f32 v121, v78, v79
	ds_read_b64_tr_b16 v[76:77], v212 offset:29696
	ds_read_b64_tr_b16 v[78:79], v212 offset:30208
	s_waitcnt lgkmcnt(12)
	v_mfma_f32_32x32x16_bf16 v[36:51], v[92:95], v[128:131], v[36:51]
	v_exp_f32_e32 v63, v63
	v_exp_f32_e32 v64, v64
	v_pk_add_f16 v0, v0, v120
	v_pk_add_f16 v84, v84, v121
	v_cvt_pk_f16_f32 v122, v80, v81
	v_cvt_pk_f16_f32 v123, v82, v83
	ds_read_b64_tr_b16 v[80:81], v212 offset:26624
	ds_read_b64_tr_b16 v[82:83], v212 offset:27136
	s_waitcnt lgkmcnt(13)
	v_mfma_f32_32x32x16_bf16 v[100:115], v[96:99], v[136:139], v[100:115]
	v_exp_f32_e32 v65, v65
	v_cvt_pk_f16_f32 v116, v52, v53
	v_pk_add_f16 v0, v0, v122
	v_pk_add_f16 v88, v84, v123
	v_cvt_pk_f16_f32 v117, v54, v55
	ds_read_b64_tr_b16 v[84:85], v212 offset:30720
	ds_read_b64_tr_b16 v[86:87], v212 offset:31232
	s_waitcnt lgkmcnt(14)
	v_mfma_f32_32x32x16_bf16 v[36:51], v[144:147], v[136:139], v[36:51]
	v_exp_f32_e32 v66, v66
	v_pk_add_f16 v0, v0, v116
	v_pk_add_f16 v52, v88, v117
	v_cvt_pk_f16_f32 v118, v56, v57
	v_cvt_pk_f16_f32 v119, v58, v59
	ds_read_b64_tr_b16 v[56:57], v212 offset:27648
	ds_read_b64_tr_b16 v[58:59], v212 offset:28160
	s_waitcnt lgkmcnt(14)
	v_mfma_f32_32x32x16_bf16 v[100:115], v[152:155], v[132:135], v[100:115]
	s_add_u32 s60, s56, 0x6c000
	s_addc_u32 s61, s57, 0
	s_add_u32 s62, s58, 0x54000
	s_addc_u32 s63, s59, 0
	v_exp_f32_e32 v67, v67
	v_cvt_pk_f16_f32 v148, v60, v61
	v_pk_add_f16 v0, v0, v118
	v_pk_add_f16 v52, v52, v119
	v_cvt_pk_f16_f32 v149, v62, v63
	ds_read_b64_tr_b16 v[60:61], v212 offset:31744
	ds_read_b64_tr_b16 v[62:63], v212 offset:32256
	v_mfma_f32_32x32x16_bf16 v[36:51], v[156:159], v[132:135], v[36:51]
	v_pk_add_f16 v0, v0, v148
	v_pk_add_f16 v174, v52, v149
	v_cvt_pk_f16_f32 v150, v64, v65
	v_cvt_pk_f16_f32 v151, v66, v67
	s_mov_b32 m0, s77
	s_nop 0
	global_load_lds_dwordx4 v165, s[60:61]
	s_mov_b32 m0, s78
	s_nop 0
	global_load_lds_dwordx4 v164, s[62:63]
	s_waitcnt lgkmcnt(14)
	v_mfma_f32_32x32x16_f16 v[4:19], v[124:127], v[160:163], v[4:19]
	v_exp_f32_e32 v100, v100
	v_exp_f32_e32 v101, v101
	v_exp_f32_e32 v102, v102
	s_waitcnt lgkmcnt(12)
	v_mfma_f32_32x32x16_f16 v[20:35], v[124:127], v[68:71], v[20:35]
	v_exp_f32_e32 v103, v103
	v_exp_f32_e32 v104, v104
	v_exp_f32_e32 v105, v105
	ds_read_b128 v[64:67], v210 offset:40960
	ds_read_b128 v[144:147], v210 offset:41472
	s_waitcnt lgkmcnt(12)
	v_mfma_f32_32x32x16_f16 v[4:19], v[120:123], v[72:75], v[4:19]
	v_exp_f32_e32 v106, v106
	v_exp_f32_e32 v107, v107
	v_exp_f32_e32 v108, v108
	ds_read_b128 v[152:155], v210 offset:43008
	ds_read_b128 v[156:159], v210 offset:43520
	s_waitcnt lgkmcnt(12)
	v_mfma_f32_32x32x16_f16 v[20:35], v[120:123], v[76:79], v[20:35]
	v_exp_f32_e32 v109, v109
	v_exp_f32_e32 v110, v110
	v_exp_f32_e32 v111, v111
	ds_read_b128 v[160:163], v210 offset:45056
	ds_read_b128 v[166:169], v210 offset:45568
	s_waitcnt lgkmcnt(12)
	v_mfma_f32_32x32x16_f16 v[4:19], v[116:119], v[80:83], v[4:19]
	v_exp_f32_e32 v112, v112
	v_exp_f32_e32 v113, v113
	v_exp_f32_e32 v114, v114
	ds_read_b128 v[170:173], v210 offset:47104
	ds_read_b128 v[52:55], v210 offset:47616
	s_waitcnt lgkmcnt(12)
	v_mfma_f32_32x32x16_f16 v[20:35], v[116:119], v[84:87], v[20:35]
	v_exp_f32_e32 v115, v115
	v_exp_f32_e32 v36, v36
	v_exp_f32_e32 v37, v37
	s_waitcnt lgkmcnt(10)
	v_mfma_f32_32x32x16_f16 v[4:19], v[148:151], v[56:59], v[4:19]
	v_exp_f32_e32 v38, v38
	v_exp_f32_e32 v39, v39
	v_exp_f32_e32 v40, v40
	s_waitcnt lgkmcnt(8)
	v_mfma_f32_32x32x16_f16 v[20:35], v[148:151], v[60:63], v[20:35]
	v_exp_f32_e32 v41, v41
	v_exp_f32_e32 v42, v42
	v_exp_f32_e32 v43, v43
	s_waitcnt vmcnt(4) lgkmcnt(0)
	s_barrier
	ds_read_b64_tr_b16 v[56:57], v212 offset:32768
	ds_read_b64_tr_b16 v[58:59], v212 offset:33280
	s_waitcnt lgkmcnt(9)
	v_mfma_f32_32x32x16_bf16 v[84:99], v[64:67], v[140:143], -4.0
	v_pk_add_f16 v0, v0, v150
	v_pk_add_f16 v60, v174, v151
	v_cvt_pk_f16_f32 v124, v100, v101
	v_pk_add_f16 v0, v0, v60
	v_cvt_pk_f16_f32 v125, v102, v103
	v_dot2c_f32_f16_e32 v2, 0x3c003c00, v0
	ds_read_b64_tr_b16 v[60:61], v212 offset:36864
	ds_read_b64_tr_b16 v[62:63], v212 offset:37376
	s_waitcnt lgkmcnt(10)
	v_mfma_f32_32x32x16_bf16 v[68:83], v[144:147], v[140:143], -4.0
	v_exp_f32_e32 v44, v44
	v_cvt_pk_f16_f32 v126, v104, v105
	v_cvt_pk_f16_f32 v127, v106, v107
	ds_read_b64_tr_b16 v[64:65], v212 offset:33792
	ds_read_b64_tr_b16 v[66:67], v212 offset:34304
	s_waitcnt lgkmcnt(11)
	v_mfma_f32_32x32x16_bf16 v[84:99], v[152:155], v[128:131], v[84:99]
	v_exp_f32_e32 v45, v45
	v_pk_add_f16 v0, v124, v126
	v_pk_add_f16 v104, v125, v127
	v_cvt_pk_f16_f32 v120, v108, v109
	v_cvt_pk_f16_f32 v121, v110, v111
	ds_read_b64_tr_b16 v[100:101], v212 offset:37888
	ds_read_b64_tr_b16 v[102:103], v212 offset:38400
	s_waitcnt lgkmcnt(12)
	v_mfma_f32_32x32x16_bf16 v[68:83], v[156:159], v[128:131], v[68:83]
	v_exp_f32_e32 v46, v46
	v_exp_f32_e32 v47, v47
	v_pk_add_f16 v0, v0, v120
	v_pk_add_f16 v108, v104, v121
	v_cvt_pk_f16_f32 v122, v112, v113
	v_cvt_pk_f16_f32 v123, v114, v115
	ds_read_b64_tr_b16 v[104:105], v212 offset:34816
	ds_read_b64_tr_b16 v[106:107], v212 offset:35328
	s_waitcnt lgkmcnt(13)
	v_mfma_f32_32x32x16_bf16 v[84:99], v[160:163], v[136:139], v[84:99]
	v_exp_f32_e32 v48, v48
	v_exp_f32_e32 v49, v49
	v_pk_add_f16 v0, v0, v122
	v_pk_add_f16 v108, v108, v123
	v_cvt_pk_f16_f32 v116, v36, v37
	v_cvt_pk_f16_f32 v117, v38, v39
	ds_read_b64_tr_b16 v[36:37], v212 offset:38912
	ds_read_b64_tr_b16 v[38:39], v212 offset:39424
	s_waitcnt lgkmcnt(14)
	v_mfma_f32_32x32x16_bf16 v[68:83], v[166:169], v[136:139], v[68:83]
	v_exp_f32_e32 v50, v50
	v_pk_add_f16 v0, v0, v116
	v_pk_add_f16 v108, v108, v117
	v_cvt_pk_f16_f32 v118, v40, v41
	v_cvt_pk_f16_f32 v119, v42, v43
	ds_read_b64_tr_b16 v[40:41], v212 offset:35840
	ds_read_b64_tr_b16 v[42:43], v212 offset:36352
	v_cvt_pk_f16_f32 v148, v44, v45
	v_pk_add_f16 v0, v0, v118
	v_pk_add_f16 v108, v108, v119
	v_cvt_pk_f16_f32 v149, v46, v47
	s_waitcnt lgkmcnt(14)
	v_mfma_f32_32x32x16_bf16 v[84:99], v[170:173], v[132:135], v[84:99]
	s_add_u32 s60, s56, 0x78000
	s_addc_u32 s61, s57, 0
	s_add_u32 s62, s58, 0x60000
	s_addc_u32 s63, s59, 0
	v_exp_f32_e32 v51, v51
	ds_read_b64_tr_b16 v[44:45], v212 offset:39936
	ds_read_b64_tr_b16 v[46:47], v212 offset:40448
	v_mfma_f32_32x32x16_bf16 v[68:83], v[52:55], v[132:135], v[68:83]
	v_pk_add_f16 v0, v0, v148
	v_pk_add_f16 v166, v108, v149
	v_cvt_pk_f16_f32 v150, v48, v49
	v_cvt_pk_f16_f32 v151, v50, v51
	s_mov_b32 m0, s79
	s_nop 0
	global_load_lds_dwordx4 v165, s[60:61]
	s_mov_b32 m0, s92
	s_nop 0
	global_load_lds_dwordx4 v164, s[62:63]
	s_waitcnt lgkmcnt(14)
	v_mfma_f32_32x32x16_f16 v[4:19], v[124:127], v[56:59], v[4:19]
	v_exp_f32_e32 v84, v84
	v_exp_f32_e32 v85, v85
	v_exp_f32_e32 v86, v86
	s_waitcnt lgkmcnt(12)
	v_mfma_f32_32x32x16_f16 v[20:35], v[124:127], v[60:63], v[20:35]
	v_exp_f32_e32 v87, v87
	v_exp_f32_e32 v88, v88
	v_exp_f32_e32 v89, v89
	ds_read_b128 v[48:51], v210
	ds_read_b128 v[108:111], v210 offset:512
	s_waitcnt lgkmcnt(12)
	v_mfma_f32_32x32x16_f16 v[4:19], v[120:123], v[64:67], v[4:19]
	v_exp_f32_e32 v90, v90
	v_exp_f32_e32 v91, v91
	v_exp_f32_e32 v92, v92
	ds_read_b128 v[112:115], v210 offset:2048
	ds_read_b128 v[144:147], v210 offset:2560
	s_waitcnt lgkmcnt(12)
	v_mfma_f32_32x32x16_f16 v[20:35], v[120:123], v[100:103], v[20:35]
	v_exp_f32_e32 v93, v93
	v_exp_f32_e32 v94, v94
	v_exp_f32_e32 v95, v95
	ds_read_b128 v[100:103], v210 offset:4096
	ds_read_b128 v[152:155], v210 offset:4608
	s_waitcnt lgkmcnt(12)
	v_mfma_f32_32x32x16_f16 v[4:19], v[116:119], v[104:107], v[4:19]
	v_exp_f32_e32 v96, v96
	v_exp_f32_e32 v97, v97
	v_exp_f32_e32 v98, v98
	ds_read_b128 v[104:107], v210 offset:6144
	ds_read_b128 v[156:159], v210 offset:6656
	s_waitcnt lgkmcnt(12)
	v_mfma_f32_32x32x16_f16 v[20:35], v[116:119], v[36:39], v[20:35]
	v_exp_f32_e32 v99, v99
	v_exp_f32_e32 v68, v68
	v_exp_f32_e32 v69, v69
	s_waitcnt lgkmcnt(10)
	v_mfma_f32_32x32x16_f16 v[4:19], v[148:151], v[40:43], v[4:19]
	v_exp_f32_e32 v70, v70
	v_exp_f32_e32 v71, v71
	v_exp_f32_e32 v72, v72
	s_waitcnt lgkmcnt(8)
	v_mfma_f32_32x32x16_f16 v[20:35], v[148:151], v[44:47], v[20:35]
	v_exp_f32_e32 v73, v73
	v_exp_f32_e32 v74, v74
	v_exp_f32_e32 v75, v75
	ds_read_b64_tr_b16 v[160:161], v212 offset:40960
	ds_read_b64_tr_b16 v[162:163], v212 offset:41472
	s_waitcnt lgkmcnt(9)
	v_mfma_f32_32x32x16_bf16 v[52:67], v[48:51], v[140:143], -4.0
	v_exp_f32_e32 v76, v76
	v_cvt_pk_f16_f32 v124, v84, v85
	v_pk_add_f16 v0, v0, v150
	v_pk_add_f16 v116, v166, v151
	v_cvt_pk_f16_f32 v125, v86, v87
	ds_read_b64_tr_b16 v[84:85], v212 offset:45056
	ds_read_b64_tr_b16 v[86:87], v212 offset:45568
	s_waitcnt lgkmcnt(10)
	v_mfma_f32_32x32x16_bf16 v[36:51], v[108:111], v[140:143], -4.0
	v_exp_f32_e32 v77, v77
	v_pk_add_f16 v0, v0, v124
	v_pk_add_f16 v108, v116, v125
	v_cvt_pk_f16_f32 v126, v88, v89
	v_cvt_pk_f16_f32 v127, v90, v91
	ds_read_b64_tr_b16 v[88:89], v212 offset:41984
	ds_read_b64_tr_b16 v[90:91], v212 offset:42496
	s_waitcnt lgkmcnt(11)
	v_mfma_f32_32x32x16_bf16 v[52:67], v[112:115], v[128:131], v[52:67]
	v_exp_f32_e32 v78, v78
	v_cvt_pk_f16_f32 v120, v92, v93
	v_pk_add_f16 v0, v0, v126
	v_pk_add_f16 v108, v108, v127
	v_cvt_pk_f16_f32 v121, v94, v95
	ds_read_b64_tr_b16 v[92:93], v212 offset:46080
	ds_read_b64_tr_b16 v[94:95], v212 offset:46592
	s_waitcnt lgkmcnt(12)
	v_mfma_f32_32x32x16_bf16 v[36:51], v[144:147], v[128:131], v[36:51]
	v_exp_f32_e32 v79, v79
	v_exp_f32_e32 v80, v80
	v_pk_add_f16 v0, v0, v120
	v_pk_add_f16 v108, v108, v121
	v_cvt_pk_f16_f32 v122, v96, v97
	v_cvt_pk_f16_f32 v123, v98, v99
	ds_read_b64_tr_b16 v[96:97], v212 offset:43008
	ds_read_b64_tr_b16 v[98:99], v212 offset:43520
	s_waitcnt lgkmcnt(13)
	v_mfma_f32_32x32x16_bf16 v[52:67], v[100:103], v[136:139], v[52:67]
	v_exp_f32_e32 v81, v81
	v_cvt_pk_f16_f32 v116, v68, v69
	v_pk_add_f16 v0, v0, v122
	v_pk_add_f16 v100, v108, v123
	v_cvt_pk_f16_f32 v117, v70, v71
	ds_read_b64_tr_b16 v[166:167], v212 offset:47104
	ds_read_b64_tr_b16 v[168:169], v212 offset:47616
	s_waitcnt lgkmcnt(14)
	v_mfma_f32_32x32x16_bf16 v[36:51], v[152:155], v[136:139], v[36:51]
	v_exp_f32_e32 v82, v82
	v_pk_add_f16 v0, v0, v116
	v_pk_add_f16 v68, v100, v117
	v_cvt_pk_f16_f32 v118, v72, v73
	v_cvt_pk_f16_f32 v119, v74, v75
	ds_read_b64_tr_b16 v[170:171], v212 offset:44032
	ds_read_b64_tr_b16 v[172:173], v212 offset:44544
	s_waitcnt lgkmcnt(14)
	v_mfma_f32_32x32x16_bf16 v[52:67], v[104:107], v[132:135], v[52:67]
	s_add_u32 s60, s56, 0x84000
	s_addc_u32 s61, s57, 0
	s_add_u32 s62, s58, 0x6c000
	s_addc_u32 s63, s59, 0
	v_exp_f32_e32 v83, v83
	v_cvt_pk_f16_f32 v148, v76, v77
	v_pk_add_f16 v0, v0, v118
	v_pk_add_f16 v68, v68, v119
	v_cvt_pk_f16_f32 v149, v78, v79
	ds_read_b64_tr_b16 v[74:75], v212 offset:48128
	ds_read_b64_tr_b16 v[76:77], v212 offset:48640
	v_mfma_f32_32x32x16_bf16 v[36:51], v[156:159], v[132:135], v[36:51]
	v_cvt_pk_f16_f32 v150, v80, v81
	v_mov_b64_e32 v[144:145], v[148:149]
	v_pk_add_f16 v72, v0, v148
	v_cvt_pk_f16_f32 v0, v82, v83
	v_mov_b64_e32 v[146:147], v[150:151]
	v_pk_add_f16 v73, v68, v149
	v_mov_b32_e32 v147, v0
	s_mov_b32 m0, s85
	s_nop 0
	global_load_lds_dwordx4 v165, s[60:61]
	s_mov_b32 m0, s93
	s_nop 0
	global_load_lds_dwordx4 v164, s[62:63]
	s_waitcnt lgkmcnt(14)
	v_mfma_f32_32x32x16_f16 v[4:19], v[124:127], v[160:163], v[4:19]
	v_exp_f32_e32 v52, v52
	v_exp_f32_e32 v53, v53
	v_exp_f32_e32 v54, v54
	s_waitcnt lgkmcnt(12)
	v_mfma_f32_32x32x16_f16 v[20:35], v[124:127], v[84:87], v[20:35]
	v_exp_f32_e32 v55, v55
	v_exp_f32_e32 v56, v56
	v_exp_f32_e32 v57, v57
	ds_read_b128 v[68:71], v210 offset:8192
	ds_read_b128 v[160:163], v210 offset:8704
	s_waitcnt lgkmcnt(12)
	v_mfma_f32_32x32x16_f16 v[4:19], v[120:123], v[88:91], v[4:19]
	v_exp_f32_e32 v58, v58
	v_exp_f32_e32 v59, v59
	v_exp_f32_e32 v60, v60
	ds_read_b128 v[156:159], v210 offset:10240
	ds_read_b128 v[112:115], v210 offset:10752
	s_waitcnt lgkmcnt(12)
	v_mfma_f32_32x32x16_f16 v[20:35], v[120:123], v[92:95], v[20:35]
	v_exp_f32_e32 v61, v61
	v_exp_f32_e32 v62, v62
	v_exp_f32_e32 v63, v63
	ds_read_b128 v[152:155], v210 offset:12288
	ds_read_b128 v[104:107], v210 offset:12800
	s_waitcnt lgkmcnt(12)
	v_mfma_f32_32x32x16_f16 v[4:19], v[116:119], v[96:99], v[4:19]
	v_exp_f32_e32 v64, v64
	v_exp_f32_e32 v65, v65
	v_exp_f32_e32 v66, v66
	ds_read_b128 v[108:111], v210 offset:14336
	ds_read_b128 v[100:103], v210 offset:14848
	s_waitcnt lgkmcnt(12)
	v_mfma_f32_32x32x16_f16 v[20:35], v[116:119], v[166:169], v[20:35]
	v_exp_f32_e32 v67, v67
	v_exp_f32_e32 v36, v36
	v_exp_f32_e32 v37, v37
	s_waitcnt lgkmcnt(10)
	v_mfma_f32_32x32x16_f16 v[4:19], v[144:147], v[170:173], v[4:19]
	v_exp_f32_e32 v38, v38
	v_exp_f32_e32 v39, v39
	v_exp_f32_e32 v40, v40
	s_waitcnt lgkmcnt(8)
	v_mfma_f32_32x32x16_f16 v[20:35], v[144:147], v[74:77], v[20:35]
	v_exp_f32_e32 v41, v41
	v_exp_f32_e32 v42, v42
	v_exp_f32_e32 v43, v43
	s_add_i32 s53, s53, 6
	s_add_u32 s54, s54, 0x48000
	s_addc_u32 s55, s55, 0
	v_mov_b32_e32 v151, v0
	s_cmpk_gt_u32 s53, 0xef
	s_waitcnt vmcnt(4) lgkmcnt(0)
	s_barrier
	s_cbranch_scc0 .LBB0_336
	v_exp_f32_e32 v44, v44
	v_exp_f32_e32 v45, v45
	v_exp_f32_e32 v46, v46
	v_exp_f32_e32 v47, v47
	v_exp_f32_e32 v48, v48
	v_exp_f32_e32 v49, v49
	v_exp_f32_e32 v50, v50
	v_exp_f32_e32 v51, v51
	s_and_b32 s11, s11, 0x3fffffc0
	s_lshl_b32 s11, s11, 2
	s_add_i32 s11, s11, 0
	s_add_i32 s11, s11, 0x18000
	ds_read_b64_tr_b16 v[148:149], v211 offset:49152
	ds_read_b64_tr_b16 v[150:151], v211 offset:49664
	s_waitcnt lgkmcnt(9)
	v_mfma_f32_32x32x16_bf16 v[84:99], v[68:71], v[140:143], -4.0
	v_mov_b32_e32 v116, v3
	v_pk_add_f16 v0, v72, v146
	v_pk_add_f16 v68, v73, v147
	v_cvt_pk_f16_f32 v124, v52, v53
	v_pk_add_f16 v0, v0, v68
	v_cvt_pk_f16_f32 v125, v54, v55
	v_dot2c_f32_f16_e32 v2, 0x3c003c00, v0
	v_mov_b32_e32 v0, v3
	ds_read_b64_tr_b16 v[52:53], v211 offset:53248
	ds_read_b64_tr_b16 v[54:55], v211 offset:53760
	s_waitcnt lgkmcnt(10)
	v_mfma_f32_32x32x16_bf16 v[68:83], v[160:163], v[140:143], -4.0
	s_nop 0
	v_pk_add_f16 v0, v0, v124
	v_pk_add_f16 v116, v116, v125
	v_cvt_pk_f16_f32 v126, v56, v57
	v_cvt_pk_f16_f32 v127, v58, v59
	ds_read_b64_tr_b16 v[56:57], v211 offset:50176
	ds_read_b64_tr_b16 v[58:59], v211 offset:50688
	s_waitcnt lgkmcnt(11)
	v_mfma_f32_32x32x16_bf16 v[84:99], v[156:159], v[128:131], v[84:99]
	v_pk_add_f16 v0, v0, v126
	v_pk_add_f16 v116, v116, v127
	v_cvt_pk_f16_f32 v120, v60, v61
	v_cvt_pk_f16_f32 v121, v62, v63
	ds_read_b64_tr_b16 v[60:61], v211 offset:54272
	ds_read_b64_tr_b16 v[62:63], v211 offset:54784
	s_waitcnt lgkmcnt(12)
	v_mfma_f32_32x32x16_bf16 v[68:83], v[112:115], v[128:131], v[68:83]
	v_pk_add_f16 v0, v0, v120
	v_pk_add_f16 v116, v116, v121
	v_cvt_pk_f16_f32 v122, v64, v65
	v_cvt_pk_f16_f32 v123, v66, v67
	ds_read_b64_tr_b16 v[64:65], v211 offset:51200
	ds_read_b64_tr_b16 v[66:67], v211 offset:51712
	s_waitcnt lgkmcnt(13)
	v_mfma_f32_32x32x16_bf16 v[84:99], v[152:155], v[136:139], v[84:99]
	v_pk_add_f16 v0, v0, v122
	v_pk_add_f16 v112, v116, v123
	v_cvt_pk_f16_f32 v116, v36, v37
	v_cvt_pk_f16_f32 v117, v38, v39
	ds_read_b64_tr_b16 v[36:37], v211 offset:55296
	ds_read_b64_tr_b16 v[38:39], v211 offset:55808
	s_waitcnt lgkmcnt(14)
	v_mfma_f32_32x32x16_bf16 v[68:83], v[104:107], v[136:139], v[68:83]
	v_pk_add_f16 v0, v0, v116
	v_pk_add_f16 v112, v112, v117
	v_cvt_pk_f16_f32 v118, v40, v41
	v_cvt_pk_f16_f32 v119, v42, v43
	ds_read_b64_tr_b16 v[40:41], v211 offset:52224
	ds_read_b64_tr_b16 v[42:43], v211 offset:52736
	s_waitcnt lgkmcnt(14)
	v_mfma_f32_32x32x16_bf16 v[84:99], v[108:111], v[132:135], v[84:99]
	v_pk_add_f16 v0, v0, v118
	v_pk_add_f16 v104, v112, v119
	v_cvt_pk_f16_f32 v144, v44, v45
	v_cvt_pk_f16_f32 v145, v46, v47
	ds_read_b64_tr_b16 v[44:45], v211 offset:56320
	ds_read_b64_tr_b16 v[46:47], v211 offset:56832
	v_mfma_f32_32x32x16_bf16 v[68:83], v[100:103], v[132:135], v[68:83]
	v_pk_add_f16 v0, v0, v144
	v_pk_add_f16 v166, v104, v145
	v_cvt_pk_f16_f32 v146, v48, v49
	v_cvt_pk_f16_f32 v147, v50, v51
	s_add_u32 s54, s88, 0xbd0000
	s_addc_u32 s55, s89, 0
	s_mov_b32 m0, s70
	s_nop 0
	global_load_lds_dwordx4 v165, s[54:55]
	s_add_u32 s54, s14, 0xbb8000
	s_addc_u32 s55, s15, 0
	s_cmp_lg_u32 0, -1
	s_cselect_b32 s53, 0, 0
	s_add_i32 s44, s53, s44
	s_add_i32 s53, s44, 0x14000
	s_mov_b32 m0, s53
	s_nop 0
	global_load_lds_dwordx4 v164, s[54:55]
	s_waitcnt lgkmcnt(14)
	v_mfma_f32_32x32x16_f16 v[4:19], v[124:127], v[148:151], v[4:19]
	v_exp_f32_e32 v84, v84
	v_exp_f32_e32 v85, v85
	v_exp_f32_e32 v86, v86
	v_exp_f32_e32 v87, v87
	s_waitcnt lgkmcnt(12)
	v_mfma_f32_32x32x16_f16 v[20:35], v[124:127], v[52:55], v[20:35]
	v_exp_f32_e32 v88, v88
	v_exp_f32_e32 v89, v89
	v_exp_f32_e32 v90, v90
	v_exp_f32_e32 v91, v91
	ds_read_b128 v[48:51], v210 offset:16384
	ds_read_b128 v[52:55], v210 offset:16896
	s_waitcnt lgkmcnt(12)
	v_mfma_f32_32x32x16_f16 v[4:19], v[120:123], v[56:59], v[4:19]
	v_exp_f32_e32 v92, v92
	v_exp_f32_e32 v93, v93
	v_exp_f32_e32 v94, v94
	v_exp_f32_e32 v95, v95
	ds_read_b128 v[56:59], v210 offset:18432
	ds_read_b128 v[148:151], v210 offset:18944
	s_waitcnt lgkmcnt(12)
	v_mfma_f32_32x32x16_f16 v[20:35], v[120:123], v[60:63], v[20:35]
	v_exp_f32_e32 v96, v96
	v_exp_f32_e32 v97, v97
	v_exp_f32_e32 v98, v98
	v_exp_f32_e32 v99, v99
	ds_read_b128 v[60:63], v210 offset:20480
	ds_read_b128 v[152:155], v210 offset:20992
	s_waitcnt lgkmcnt(12)
	v_mfma_f32_32x32x16_f16 v[4:19], v[116:119], v[64:67], v[4:19]
	v_exp_f32_e32 v68, v68
	v_exp_f32_e32 v69, v69
	v_exp_f32_e32 v70, v70
	v_exp_f32_e32 v71, v71
	ds_read_b128 v[64:67], v210 offset:22528
	ds_read_b128 v[156:159], v210 offset:23040
	s_waitcnt lgkmcnt(12)
	v_mfma_f32_32x32x16_f16 v[20:35], v[116:119], v[36:39], v[20:35]
	v_exp_f32_e32 v72, v72
	v_exp_f32_e32 v73, v73
	v_exp_f32_e32 v74, v74
	v_exp_f32_e32 v75, v75
	s_waitcnt lgkmcnt(10)
	v_mfma_f32_32x32x16_f16 v[4:19], v[144:147], v[40:43], v[4:19]
	v_exp_f32_e32 v76, v76
	v_exp_f32_e32 v77, v77
	v_exp_f32_e32 v78, v78
	v_exp_f32_e32 v79, v79
	s_waitcnt lgkmcnt(8)
	v_mfma_f32_32x32x16_f16 v[20:35], v[144:147], v[44:47], v[20:35]
	v_exp_f32_e32 v80, v80
	v_exp_f32_e32 v81, v81
	v_exp_f32_e32 v82, v82
	v_exp_f32_e32 v83, v83
	ds_read_b64_tr_b16 v[160:161], v211 offset:57344
	ds_read_b64_tr_b16 v[162:163], v211 offset:57856
	s_waitcnt lgkmcnt(9)
	v_mfma_f32_32x32x16_bf16 v[100:115], v[48:51], v[140:143], -4.0
	v_cvt_pk_f16_f32 v124, v84, v85
	v_pk_add_f16 v0, v0, v146
	v_pk_add_f16 v116, v166, v147
	v_cvt_pk_f16_f32 v125, v86, v87
	ds_read_b64_tr_b16 v[84:85], v211 offset:61440
	ds_read_b64_tr_b16 v[86:87], v211 offset:61952
	s_waitcnt lgkmcnt(10)
	v_mfma_f32_32x32x16_bf16 v[36:51], v[52:55], v[140:143], -4.0
	s_nop 0
	v_pk_add_f16 v0, v0, v124
	v_pk_add_f16 v116, v116, v125
	v_cvt_pk_f16_f32 v126, v88, v89
	v_cvt_pk_f16_f32 v127, v90, v91
	ds_read_b64_tr_b16 v[52:53], v211 offset:58368
	ds_read_b64_tr_b16 v[54:55], v211 offset:58880
	s_waitcnt lgkmcnt(11)
	v_mfma_f32_32x32x16_bf16 v[100:115], v[56:59], v[128:131], v[100:115]
	v_pk_add_f16 v0, v0, v126
	v_pk_add_f16 v88, v116, v127
	v_cvt_pk_f16_f32 v120, v92, v93
	v_cvt_pk_f16_f32 v121, v94, v95
	ds_read_b64_tr_b16 v[56:57], v211 offset:62464
	ds_read_b64_tr_b16 v[58:59], v211 offset:62976
	s_waitcnt lgkmcnt(12)
	v_mfma_f32_32x32x16_bf16 v[36:51], v[148:151], v[128:131], v[36:51]
	s_nop 0
	v_pk_add_f16 v0, v0, v120
	v_pk_add_f16 v92, v88, v121
	v_cvt_pk_f16_f32 v122, v96, v97
	v_cvt_pk_f16_f32 v123, v98, v99
	ds_read_b64_tr_b16 v[88:89], v211 offset:59392
	ds_read_b64_tr_b16 v[90:91], v211 offset:59904
	s_waitcnt lgkmcnt(13)
	v_mfma_f32_32x32x16_bf16 v[100:115], v[60:63], v[136:139], v[100:115]
	v_pk_add_f16 v0, v0, v122
	v_pk_add_f16 v92, v92, v123
	v_cvt_pk_f16_f32 v116, v68, v69
	v_cvt_pk_f16_f32 v117, v70, v71
	ds_read_b64_tr_b16 v[60:61], v211 offset:63488
	ds_read_b64_tr_b16 v[62:63], v211 offset:64000
	s_waitcnt lgkmcnt(14)
	v_mfma_f32_32x32x16_bf16 v[36:51], v[152:155], v[136:139], v[36:51]
	s_nop 0
	v_pk_add_f16 v0, v0, v116
	v_pk_add_f16 v68, v92, v117
	v_cvt_pk_f16_f32 v118, v72, v73
	v_cvt_pk_f16_f32 v119, v74, v75
	ds_read_b64_tr_b16 v[72:73], v211 offset:60416
	ds_read_b64_tr_b16 v[74:75], v211 offset:60928
	s_waitcnt lgkmcnt(14)
	v_mfma_f32_32x32x16_bf16 v[100:115], v[64:67], v[132:135], v[100:115]
	v_pk_add_f16 v0, v0, v118
	v_pk_add_f16 v68, v68, v119
	v_cvt_pk_f16_f32 v144, v76, v77
	v_cvt_pk_f16_f32 v145, v78, v79
	ds_read_b64_tr_b16 v[64:65], v211 offset:64512
	ds_read_b64_tr_b16 v[66:67], v211 offset:65024
	v_mfma_f32_32x32x16_bf16 v[36:51], v[156:159], v[132:135], v[36:51]
	s_nop 0
	v_pk_add_f16 v0, v0, v144
	v_pk_add_f16 v170, v68, v145
	v_cvt_pk_f16_f32 v146, v80, v81
	v_cvt_pk_f16_f32 v147, v82, v83
	s_add_u32 s54, s88, 0xbdc000
	s_addc_u32 s55, s89, 0
	s_add_i32 s53, s44, 0x2000
	s_mov_b32 m0, s53
	s_nop 0
	global_load_lds_dwordx4 v165, s[54:55]
	s_add_u32 s54, s14, 0xbc4000
	s_addc_u32 s55, s15, 0
	s_add_i32 s53, s44, 0x16000
	s_mov_b32 m0, s53
	s_nop 0
	global_load_lds_dwordx4 v164, s[54:55]
	s_waitcnt lgkmcnt(14)
	v_mfma_f32_32x32x16_f16 v[4:19], v[124:127], v[160:163], v[4:19]
	v_exp_f32_e32 v100, v100
	v_exp_f32_e32 v101, v101
	v_exp_f32_e32 v102, v102
	v_exp_f32_e32 v103, v103
	s_waitcnt lgkmcnt(12)
	v_mfma_f32_32x32x16_f16 v[20:35], v[124:127], v[84:87], v[20:35]
	v_exp_f32_e32 v104, v104
	v_exp_f32_e32 v105, v105
	v_exp_f32_e32 v106, v106
	v_exp_f32_e32 v107, v107
	ds_read_b128 v[76:79], v210 offset:24576
	ds_read_b128 v[80:83], v210 offset:25088
	s_waitcnt lgkmcnt(12)
	v_mfma_f32_32x32x16_f16 v[4:19], v[120:123], v[52:55], v[4:19]
	v_exp_f32_e32 v108, v108
	v_exp_f32_e32 v109, v109
	v_exp_f32_e32 v110, v110
	v_exp_f32_e32 v111, v111
	ds_read_b128 v[148:151], v210 offset:26624
	ds_read_b128 v[152:155], v210 offset:27136
	s_waitcnt lgkmcnt(12)
	v_mfma_f32_32x32x16_f16 v[20:35], v[120:123], v[56:59], v[20:35]
	v_exp_f32_e32 v112, v112
	v_exp_f32_e32 v113, v113
	v_exp_f32_e32 v114, v114
	v_exp_f32_e32 v115, v115
	ds_read_b128 v[156:159], v210 offset:28672
	ds_read_b128 v[160:163], v210 offset:29184
	s_waitcnt lgkmcnt(12)
	v_mfma_f32_32x32x16_f16 v[4:19], v[116:119], v[88:91], v[4:19]
	v_exp_f32_e32 v36, v36
	v_exp_f32_e32 v37, v37
	v_exp_f32_e32 v38, v38
	v_exp_f32_e32 v39, v39
	ds_read_b128 v[166:169], v210 offset:30720
	ds_read_b128 v[68:71], v210 offset:31232
	s_waitcnt lgkmcnt(12)
	v_mfma_f32_32x32x16_f16 v[20:35], v[116:119], v[60:63], v[20:35]
	v_exp_f32_e32 v40, v40
	v_exp_f32_e32 v41, v41
	v_exp_f32_e32 v42, v42
	v_exp_f32_e32 v43, v43
	s_waitcnt lgkmcnt(10)
	v_mfma_f32_32x32x16_f16 v[4:19], v[144:147], v[72:75], v[4:19]
	v_exp_f32_e32 v44, v44
	v_exp_f32_e32 v45, v45
	v_exp_f32_e32 v46, v46
	v_exp_f32_e32 v47, v47
	s_waitcnt lgkmcnt(8)
	v_mfma_f32_32x32x16_f16 v[20:35], v[144:147], v[64:67], v[20:35]
	v_exp_f32_e32 v48, v48
	v_exp_f32_e32 v49, v49
	v_exp_f32_e32 v50, v50
	v_exp_f32_e32 v51, v51
	s_waitcnt vmcnt(4) lgkmcnt(0)
	s_barrier
	ds_read_b64_tr_b16 v[72:73], v212 offset:16384
	ds_read_b64_tr_b16 v[74:75], v212 offset:16896
	s_waitcnt lgkmcnt(9)
	v_mfma_f32_32x32x16_bf16 v[84:99], v[76:79], v[140:143], -4.0
	v_cvt_pk_f16_f32 v124, v100, v101
	v_pk_add_f16 v0, v0, v146
	v_pk_add_f16 v52, v170, v147
	v_mov_b32_e32 v100, v3
	v_pk_add_f16 v0, v0, v52
	v_cvt_pk_f16_f32 v125, v102, v103
	v_dot2c_f32_f16_e32 v2, 0x3c003c00, v0
	v_mov_b32_e32 v0, v3
	ds_read_b64_tr_b16 v[76:77], v212 offset:20480
	ds_read_b64_tr_b16 v[78:79], v212 offset:20992
	s_waitcnt lgkmcnt(10)
	v_mfma_f32_32x32x16_bf16 v[52:67], v[80:83], v[140:143], -4.0
	s_nop 0
	v_pk_add_f16 v0, v0, v124
	v_pk_add_f16 v100, v100, v125
	v_cvt_pk_f16_f32 v126, v104, v105
	v_cvt_pk_f16_f32 v127, v106, v107
	ds_read_b64_tr_b16 v[80:81], v212 offset:17408
	ds_read_b64_tr_b16 v[82:83], v212 offset:17920
	s_waitcnt lgkmcnt(11)
	v_mfma_f32_32x32x16_bf16 v[84:99], v[148:151], v[128:131], v[84:99]
	v_pk_add_f16 v0, v0, v126
	v_pk_add_f16 v104, v100, v127
	v_cvt_pk_f16_f32 v120, v108, v109
	v_cvt_pk_f16_f32 v121, v110, v111
	ds_read_b64_tr_b16 v[100:101], v212 offset:21504
	ds_read_b64_tr_b16 v[102:103], v212 offset:22016
	s_waitcnt lgkmcnt(12)
	v_mfma_f32_32x32x16_bf16 v[52:67], v[152:155], v[128:131], v[52:67]
	v_pk_add_f16 v0, v0, v120
	v_pk_add_f16 v108, v104, v121
	v_cvt_pk_f16_f32 v122, v112, v113
	v_cvt_pk_f16_f32 v123, v114, v115
	ds_read_b64_tr_b16 v[104:105], v212 offset:18432
	ds_read_b64_tr_b16 v[106:107], v212 offset:18944
	s_waitcnt lgkmcnt(13)
	v_mfma_f32_32x32x16_bf16 v[84:99], v[156:159], v[136:139], v[84:99]
	v_pk_add_f16 v0, v0, v122
	v_pk_add_f16 v108, v108, v123
	v_cvt_pk_f16_f32 v116, v36, v37
	v_cvt_pk_f16_f32 v117, v38, v39
	ds_read_b64_tr_b16 v[36:37], v212 offset:22528
	ds_read_b64_tr_b16 v[38:39], v212 offset:23040
	s_waitcnt lgkmcnt(14)
	v_mfma_f32_32x32x16_bf16 v[52:67], v[160:163], v[136:139], v[52:67]
	v_pk_add_f16 v0, v0, v116
	v_pk_add_f16 v108, v108, v117
	v_cvt_pk_f16_f32 v118, v40, v41
	v_cvt_pk_f16_f32 v119, v42, v43
	ds_read_b64_tr_b16 v[40:41], v212 offset:19456
	ds_read_b64_tr_b16 v[42:43], v212 offset:19968
	s_waitcnt lgkmcnt(14)
	v_mfma_f32_32x32x16_bf16 v[84:99], v[166:169], v[132:135], v[84:99]
	v_pk_add_f16 v0, v0, v118
	v_pk_add_f16 v108, v108, v119
	v_cvt_pk_f16_f32 v144, v44, v45
	v_cvt_pk_f16_f32 v145, v46, v47
	ds_read_b64_tr_b16 v[44:45], v212 offset:23552
	ds_read_b64_tr_b16 v[46:47], v212 offset:24064
	v_mfma_f32_32x32x16_bf16 v[52:67], v[68:71], v[132:135], v[52:67]
	v_pk_add_f16 v0, v0, v144
	v_pk_add_f16 v166, v108, v145
	v_cvt_pk_f16_f32 v146, v48, v49
	v_cvt_pk_f16_f32 v147, v50, v51
	s_add_u32 s54, s88, 0xbe8000
	s_addc_u32 s55, s89, 0
	s_add_i32 s53, s44, 0x4000
	s_mov_b32 m0, s53
	s_nop 0
	global_load_lds_dwordx4 v165, s[54:55]
	s_add_u32 s54, s14, 0xbd0000
	s_addc_u32 s55, s15, 0
	s_mov_b32 m0, s10
	s_nop 0
	global_load_lds_dwordx4 v164, s[54:55]
	s_waitcnt lgkmcnt(14)
	v_mfma_f32_32x32x16_f16 v[4:19], v[124:127], v[72:75], v[4:19]
	v_exp_f32_e32 v84, v84
	v_exp_f32_e32 v85, v85
	v_exp_f32_e32 v86, v86
	v_exp_f32_e32 v87, v87
	s_waitcnt lgkmcnt(12)
	v_mfma_f32_32x32x16_f16 v[20:35], v[124:127], v[76:79], v[20:35]
	v_exp_f32_e32 v88, v88
	v_exp_f32_e32 v89, v89
	v_exp_f32_e32 v90, v90
	v_exp_f32_e32 v91, v91
	ds_read_b128 v[48:51], v210 offset:32768
	ds_read_b128 v[108:111], v210 offset:33280
	s_waitcnt lgkmcnt(12)
	v_mfma_f32_32x32x16_f16 v[4:19], v[120:123], v[80:83], v[4:19]
	v_exp_f32_e32 v92, v92
	v_exp_f32_e32 v93, v93
	v_exp_f32_e32 v94, v94
	v_exp_f32_e32 v95, v95
	ds_read_b128 v[112:115], v210 offset:34816
	ds_read_b128 v[148:151], v210 offset:35328
	s_waitcnt lgkmcnt(12)
	v_mfma_f32_32x32x16_f16 v[20:35], v[120:123], v[100:103], v[20:35]
	v_exp_f32_e32 v96, v96
	v_exp_f32_e32 v97, v97
	v_exp_f32_e32 v98, v98
	v_exp_f32_e32 v99, v99
	ds_read_b128 v[100:103], v210 offset:36864
	ds_read_b128 v[152:155], v210 offset:37376
	s_waitcnt lgkmcnt(12)
	v_mfma_f32_32x32x16_f16 v[4:19], v[116:119], v[104:107], v[4:19]
	v_exp_f32_e32 v52, v52
	v_exp_f32_e32 v53, v53
	v_exp_f32_e32 v54, v54
	v_exp_f32_e32 v55, v55
	ds_read_b128 v[104:107], v210 offset:38912
	ds_read_b128 v[156:159], v210 offset:39424
	s_waitcnt lgkmcnt(12)
	v_mfma_f32_32x32x16_f16 v[20:35], v[116:119], v[36:39], v[20:35]
	v_exp_f32_e32 v56, v56
	v_exp_f32_e32 v57, v57
	v_exp_f32_e32 v58, v58
	v_exp_f32_e32 v59, v59
	s_waitcnt lgkmcnt(10)
	v_mfma_f32_32x32x16_f16 v[4:19], v[144:147], v[40:43], v[4:19]
	v_exp_f32_e32 v60, v60
	v_exp_f32_e32 v61, v61
	v_exp_f32_e32 v62, v62
	v_exp_f32_e32 v63, v63
	s_waitcnt lgkmcnt(8)
	v_mfma_f32_32x32x16_f16 v[20:35], v[144:147], v[44:47], v[20:35]
	v_exp_f32_e32 v64, v64
	v_exp_f32_e32 v65, v65
	v_exp_f32_e32 v66, v66
	v_exp_f32_e32 v67, v67
	ds_read_b64_tr_b16 v[160:161], v212 offset:24576
	ds_read_b64_tr_b16 v[162:163], v212 offset:25088
	s_waitcnt lgkmcnt(9)
	v_mfma_f32_32x32x16_bf16 v[68:83], v[48:51], v[140:143], -4.0
	v_cvt_pk_f16_f32 v124, v84, v85
	v_pk_add_f16 v0, v0, v146
	v_pk_add_f16 v116, v166, v147
	v_cvt_pk_f16_f32 v125, v86, v87
	ds_read_b64_tr_b16 v[84:85], v212 offset:28672
	ds_read_b64_tr_b16 v[86:87], v212 offset:29184
	s_waitcnt lgkmcnt(10)
	v_mfma_f32_32x32x16_bf16 v[36:51], v[108:111], v[140:143], -4.0
	s_nop 0
	v_pk_add_f16 v0, v0, v124
	v_pk_add_f16 v108, v116, v125
	v_cvt_pk_f16_f32 v126, v88, v89
	v_cvt_pk_f16_f32 v127, v90, v91
	ds_read_b64_tr_b16 v[88:89], v212 offset:25600
	ds_read_b64_tr_b16 v[90:91], v212 offset:26112
	s_waitcnt lgkmcnt(11)
	v_mfma_f32_32x32x16_bf16 v[68:83], v[112:115], v[128:131], v[68:83]
	v_pk_add_f16 v0, v0, v126
	v_pk_add_f16 v108, v108, v127
	v_cvt_pk_f16_f32 v120, v92, v93
	v_cvt_pk_f16_f32 v121, v94, v95
	ds_read_b64_tr_b16 v[92:93], v212 offset:29696
	ds_read_b64_tr_b16 v[94:95], v212 offset:30208
	s_waitcnt lgkmcnt(12)
	v_mfma_f32_32x32x16_bf16 v[36:51], v[148:151], v[128:131], v[36:51]
	s_nop 0
	v_pk_add_f16 v0, v0, v120
	v_pk_add_f16 v108, v108, v121
	v_cvt_pk_f16_f32 v122, v96, v97
	v_cvt_pk_f16_f32 v123, v98, v99
	ds_read_b64_tr_b16 v[96:97], v212 offset:26624
	ds_read_b64_tr_b16 v[98:99], v212 offset:27136
	s_waitcnt lgkmcnt(13)
	v_mfma_f32_32x32x16_bf16 v[68:83], v[100:103], v[136:139], v[68:83]
	v_cvt_pk_f16_f32 v116, v52, v53
	v_pk_add_f16 v0, v0, v122
	v_pk_add_f16 v100, v108, v123
	v_cvt_pk_f16_f32 v117, v54, v55
	ds_read_b64_tr_b16 v[52:53], v212 offset:30720
	ds_read_b64_tr_b16 v[54:55], v212 offset:31232
	s_waitcnt lgkmcnt(14)
	v_mfma_f32_32x32x16_bf16 v[36:51], v[152:155], v[136:139], v[36:51]
	s_nop 0
	v_pk_add_f16 v0, v0, v116
	v_pk_add_f16 v100, v100, v117
	v_cvt_pk_f16_f32 v118, v56, v57
	v_cvt_pk_f16_f32 v119, v58, v59
	ds_read_b64_tr_b16 v[56:57], v212 offset:27648
	ds_read_b64_tr_b16 v[58:59], v212 offset:28160
	s_waitcnt lgkmcnt(14)
	v_mfma_f32_32x32x16_bf16 v[68:83], v[104:107], v[132:135], v[68:83]
	v_pk_add_f16 v0, v0, v118
	v_pk_add_f16 v100, v100, v119
	v_cvt_pk_f16_f32 v144, v60, v61
	v_cvt_pk_f16_f32 v145, v62, v63
	ds_read_b64_tr_b16 v[60:61], v212 offset:31744
	ds_read_b64_tr_b16 v[62:63], v212 offset:32256
	v_mfma_f32_32x32x16_bf16 v[36:51], v[156:159], v[132:135], v[36:51]
	s_nop 0
	v_pk_add_f16 v0, v0, v144
	v_pk_add_f16 v166, v100, v145
	v_cvt_pk_f16_f32 v146, v64, v65
	v_cvt_pk_f16_f32 v147, v66, v67
	s_add_u32 s54, s88, 0xbf4000
	s_addc_u32 s55, s89, 0
	s_add_i32 s10, s44, 0x6000
	s_mov_b32 m0, s10
	s_nop 0
	global_load_lds_dwordx4 v165, s[54:55]
	s_add_u32 s54, s14, 0xbdc000
	s_addc_u32 s55, s15, 0
	s_add_i32 s10, s44, 0xe000
	s_mov_b32 m0, s10
	s_nop 0
	global_load_lds_dwordx4 v164, s[54:55]
	s_waitcnt lgkmcnt(14)
	v_mfma_f32_32x32x16_f16 v[4:19], v[124:127], v[160:163], v[4:19]
	v_exp_f32_e32 v68, v68
	v_exp_f32_e32 v69, v69
	v_exp_f32_e32 v70, v70
	v_exp_f32_e32 v71, v71
	s_waitcnt lgkmcnt(12)
	v_mfma_f32_32x32x16_f16 v[20:35], v[124:127], v[84:87], v[20:35]
	v_exp_f32_e32 v72, v72
	v_exp_f32_e32 v73, v73
	v_exp_f32_e32 v74, v74
	v_exp_f32_e32 v75, v75
	ds_read_b128 v[64:67], v210 offset:40960
	ds_read_b128 v[104:107], v210 offset:41472
	s_waitcnt lgkmcnt(12)
	v_mfma_f32_32x32x16_f16 v[4:19], v[120:123], v[88:91], v[4:19]
	v_exp_f32_e32 v76, v76
	v_exp_f32_e32 v77, v77
	v_exp_f32_e32 v78, v78
	v_exp_f32_e32 v79, v79
	ds_read_b128 v[108:111], v210 offset:43008
	ds_read_b128 v[112:115], v210 offset:43520
	s_waitcnt lgkmcnt(12)
	v_mfma_f32_32x32x16_f16 v[20:35], v[120:123], v[92:95], v[20:35]
	v_exp_f32_e32 v80, v80
	v_exp_f32_e32 v81, v81
	v_exp_f32_e32 v82, v82
	v_exp_f32_e32 v83, v83
	ds_read_b128 v[148:151], v210 offset:45056
	ds_read_b128 v[152:155], v210 offset:45568
	s_waitcnt lgkmcnt(12)
	v_mfma_f32_32x32x16_f16 v[4:19], v[116:119], v[96:99], v[4:19]
	v_exp_f32_e32 v36, v36
	v_exp_f32_e32 v37, v37
	v_exp_f32_e32 v38, v38
	v_exp_f32_e32 v39, v39
	ds_read_b128 v[156:159], v210 offset:47104
	ds_read_b128 v[100:103], v210 offset:47616
	s_waitcnt lgkmcnt(12)
	v_mfma_f32_32x32x16_f16 v[20:35], v[116:119], v[52:55], v[20:35]
	v_exp_f32_e32 v40, v40
	v_exp_f32_e32 v41, v41
	v_exp_f32_e32 v42, v42
	v_exp_f32_e32 v43, v43
	s_waitcnt lgkmcnt(10)
	v_mfma_f32_32x32x16_f16 v[4:19], v[144:147], v[56:59], v[4:19]
	v_exp_f32_e32 v44, v44
	v_exp_f32_e32 v45, v45
	v_exp_f32_e32 v46, v46
	v_exp_f32_e32 v47, v47
	s_waitcnt lgkmcnt(8)
	v_mfma_f32_32x32x16_f16 v[20:35], v[144:147], v[60:63], v[20:35]
	v_exp_f32_e32 v48, v48
	v_exp_f32_e32 v49, v49
	v_exp_f32_e32 v50, v50
	v_exp_f32_e32 v51, v51
	s_waitcnt vmcnt(4) lgkmcnt(0)
	s_barrier
	ds_read_b64_tr_b16 v[160:161], v212 offset:32768
	ds_read_b64_tr_b16 v[162:163], v212 offset:33280
	s_waitcnt lgkmcnt(9)
	v_mfma_f32_32x32x16_bf16 v[84:99], v[64:67], v[140:143], -4.0
	v_mov_b32_e32 v116, v3
	v_pk_add_f16 v0, v0, v146
	v_pk_add_f16 v52, v166, v147
	v_cvt_pk_f16_f32 v124, v68, v69
	v_pk_add_f16 v0, v0, v52
	v_cvt_pk_f16_f32 v125, v70, v71
	v_dot2c_f32_f16_e32 v2, 0x3c003c00, v0
	v_mov_b32_e32 v0, v3
	ds_read_b64_tr_b16 v[68:69], v212 offset:36864
	ds_read_b64_tr_b16 v[70:71], v212 offset:37376
	s_waitcnt lgkmcnt(10)
	v_mfma_f32_32x32x16_bf16 v[52:67], v[104:107], v[140:143], -4.0
	s_nop 0
	v_pk_add_f16 v0, v0, v124
	v_pk_add_f16 v104, v116, v125
	v_cvt_pk_f16_f32 v126, v72, v73
	v_cvt_pk_f16_f32 v127, v74, v75
	ds_read_b64_tr_b16 v[72:73], v212 offset:33792
	ds_read_b64_tr_b16 v[74:75], v212 offset:34304
	s_waitcnt lgkmcnt(11)
	v_mfma_f32_32x32x16_bf16 v[84:99], v[108:111], v[128:131], v[84:99]
	v_pk_add_f16 v0, v0, v126
	v_pk_add_f16 v104, v104, v127
	v_cvt_pk_f16_f32 v120, v76, v77
	v_cvt_pk_f16_f32 v121, v78, v79
	ds_read_b64_tr_b16 v[76:77], v212 offset:37888
	ds_read_b64_tr_b16 v[78:79], v212 offset:38400
	s_waitcnt lgkmcnt(12)
	v_mfma_f32_32x32x16_bf16 v[52:67], v[112:115], v[128:131], v[52:67]
	v_pk_add_f16 v0, v0, v120
	v_pk_add_f16 v104, v104, v121
	v_cvt_pk_f16_f32 v122, v80, v81
	v_cvt_pk_f16_f32 v123, v82, v83
	ds_read_b64_tr_b16 v[80:81], v212 offset:34816
	ds_read_b64_tr_b16 v[82:83], v212 offset:35328
	s_waitcnt lgkmcnt(13)
	v_mfma_f32_32x32x16_bf16 v[84:99], v[148:151], v[136:139], v[84:99]
	v_pk_add_f16 v0, v0, v122
	v_pk_add_f16 v104, v104, v123
	v_cvt_pk_f16_f32 v116, v36, v37
	v_cvt_pk_f16_f32 v117, v38, v39
	ds_read_b64_tr_b16 v[36:37], v212 offset:38912
	ds_read_b64_tr_b16 v[38:39], v212 offset:39424
	s_waitcnt lgkmcnt(14)
	v_mfma_f32_32x32x16_bf16 v[52:67], v[152:155], v[136:139], v[52:67]
	v_pk_add_f16 v0, v0, v116
	v_pk_add_f16 v104, v104, v117
	v_cvt_pk_f16_f32 v118, v40, v41
	v_cvt_pk_f16_f32 v119, v42, v43
	ds_read_b64_tr_b16 v[40:41], v212 offset:35840
	ds_read_b64_tr_b16 v[42:43], v212 offset:36352
	s_waitcnt lgkmcnt(14)
	v_mfma_f32_32x32x16_bf16 v[84:99], v[156:159], v[132:135], v[84:99]
	v_pk_add_f16 v0, v0, v118
	v_pk_add_f16 v104, v104, v119
	v_cvt_pk_f16_f32 v144, v44, v45
	v_cvt_pk_f16_f32 v145, v46, v47
	ds_read_b64_tr_b16 v[44:45], v212 offset:39936
	ds_read_b64_tr_b16 v[46:47], v212 offset:40448
	v_mfma_f32_32x32x16_bf16 v[52:67], v[100:103], v[132:135], v[52:67]
	v_pk_add_f16 v0, v0, v144
	v_pk_add_f16 v165, v104, v145
	v_cvt_pk_f16_f32 v146, v48, v49
	v_cvt_pk_f16_f32 v147, v50, v51
	s_add_u32 s54, s14, 0xbe8000
	s_addc_u32 s55, s15, 0
	s_add_i32 s10, s44, 0x10000
	s_mov_b32 m0, s10
	s_nop 0
	global_load_lds_dwordx4 v164, s[54:55]
	s_waitcnt lgkmcnt(14)
	v_mfma_f32_32x32x16_f16 v[4:19], v[124:127], v[160:163], v[4:19]
	v_exp_f32_e32 v84, v84
	v_exp_f32_e32 v85, v85
	v_exp_f32_e32 v86, v86
	v_exp_f32_e32 v87, v87
	s_waitcnt lgkmcnt(12)
	v_mfma_f32_32x32x16_f16 v[20:35], v[124:127], v[68:71], v[20:35]
	v_exp_f32_e32 v88, v88
	v_exp_f32_e32 v89, v89
	v_exp_f32_e32 v90, v90
	v_exp_f32_e32 v91, v91
	ds_read_b128 v[48:51], v210
	ds_read_b128 v[100:103], v210 offset:512
	s_waitcnt lgkmcnt(12)
	v_mfma_f32_32x32x16_f16 v[4:19], v[120:123], v[72:75], v[4:19]
	v_exp_f32_e32 v92, v92
	v_exp_f32_e32 v93, v93
	v_exp_f32_e32 v94, v94
	v_exp_f32_e32 v95, v95
	ds_read_b128 v[104:107], v210 offset:2048
	ds_read_b128 v[108:111], v210 offset:2560
	s_waitcnt lgkmcnt(12)
	v_mfma_f32_32x32x16_f16 v[20:35], v[120:123], v[76:79], v[20:35]
	v_exp_f32_e32 v96, v96
	v_exp_f32_e32 v97, v97
	v_exp_f32_e32 v98, v98
	v_exp_f32_e32 v99, v99
	ds_read_b128 v[112:115], v210 offset:4096
	ds_read_b128 v[148:151], v210 offset:4608
	s_waitcnt lgkmcnt(12)
	v_mfma_f32_32x32x16_f16 v[4:19], v[116:119], v[80:83], v[4:19]
	v_exp_f32_e32 v52, v52
	v_exp_f32_e32 v53, v53
	v_exp_f32_e32 v54, v54
	v_exp_f32_e32 v55, v55
	ds_read_b128 v[152:155], v210 offset:6144
	ds_read_b128 v[156:159], v210 offset:6656
	s_waitcnt lgkmcnt(12)
	v_mfma_f32_32x32x16_f16 v[20:35], v[116:119], v[36:39], v[20:35]
	v_exp_f32_e32 v56, v56
	v_exp_f32_e32 v57, v57
	v_exp_f32_e32 v58, v58
	v_exp_f32_e32 v59, v59
	s_waitcnt lgkmcnt(10)
	v_mfma_f32_32x32x16_f16 v[4:19], v[144:147], v[40:43], v[4:19]
	v_exp_f32_e32 v60, v60
	v_exp_f32_e32 v61, v61
	v_exp_f32_e32 v62, v62
	v_exp_f32_e32 v63, v63
	s_waitcnt lgkmcnt(8)
	v_mfma_f32_32x32x16_f16 v[20:35], v[144:147], v[44:47], v[20:35]
	v_exp_f32_e32 v64, v64
	v_exp_f32_e32 v65, v65
	v_exp_f32_e32 v66, v66
	v_exp_f32_e32 v67, v67
	ds_read_b64_tr_b16 v[160:161], v212 offset:40960
	ds_read_b64_tr_b16 v[162:163], v212 offset:41472
	s_waitcnt lgkmcnt(9)
	v_mfma_f32_32x32x16_bf16 v[68:83], v[48:51], v[140:143], -4.0
	v_cvt_pk_f16_f32 v124, v84, v85
	v_pk_add_f16 v0, v0, v146
	v_pk_add_f16 v116, v165, v147
	v_cvt_pk_f16_f32 v125, v86, v87
	ds_read_b64_tr_b16 v[84:85], v212 offset:45056
	ds_read_b64_tr_b16 v[86:87], v212 offset:45568
	s_waitcnt lgkmcnt(10)
	v_mfma_f32_32x32x16_bf16 v[36:51], v[100:103], v[140:143], -4.0
	s_nop 0
	v_pk_add_f16 v0, v0, v124
	v_pk_add_f16 v100, v116, v125
	v_cvt_pk_f16_f32 v126, v88, v89
	v_cvt_pk_f16_f32 v127, v90, v91
	ds_read_b64_tr_b16 v[88:89], v212 offset:41984
	ds_read_b64_tr_b16 v[90:91], v212 offset:42496
	s_waitcnt lgkmcnt(11)
	v_mfma_f32_32x32x16_bf16 v[68:83], v[104:107], v[128:131], v[68:83]
	v_pk_add_f16 v0, v0, v126
	v_pk_add_f16 v100, v100, v127
	v_cvt_pk_f16_f32 v120, v92, v93
	v_cvt_pk_f16_f32 v121, v94, v95
	ds_read_b64_tr_b16 v[92:93], v212 offset:46080
	ds_read_b64_tr_b16 v[94:95], v212 offset:46592
	s_waitcnt lgkmcnt(12)
	v_mfma_f32_32x32x16_bf16 v[36:51], v[108:111], v[128:131], v[36:51]
	s_nop 0
	v_pk_add_f16 v0, v0, v120
	v_pk_add_f16 v100, v100, v121
	v_cvt_pk_f16_f32 v122, v96, v97
	v_cvt_pk_f16_f32 v123, v98, v99
	ds_read_b64_tr_b16 v[96:97], v212 offset:43008
	ds_read_b64_tr_b16 v[98:99], v212 offset:43520
	s_waitcnt lgkmcnt(13)
	v_mfma_f32_32x32x16_bf16 v[68:83], v[112:115], v[136:139], v[68:83]
	v_pk_add_f16 v0, v0, v122
	v_pk_add_f16 v100, v100, v123
	v_cvt_pk_f16_f32 v116, v52, v53
	v_cvt_pk_f16_f32 v117, v54, v55
	ds_read_b64_tr_b16 v[52:53], v212 offset:47104
	ds_read_b64_tr_b16 v[54:55], v212 offset:47616
	s_waitcnt lgkmcnt(14)
	v_mfma_f32_32x32x16_bf16 v[36:51], v[148:151], v[136:139], v[36:51]
	s_nop 0
	v_pk_add_f16 v0, v0, v116
	v_pk_add_f16 v100, v100, v117
	v_cvt_pk_f16_f32 v118, v56, v57
	v_cvt_pk_f16_f32 v119, v58, v59
	ds_read_b64_tr_b16 v[56:57], v212 offset:44032
	ds_read_b64_tr_b16 v[58:59], v212 offset:44544
	s_waitcnt lgkmcnt(14)
	v_mfma_f32_32x32x16_bf16 v[68:83], v[152:155], v[132:135], v[68:83]
	v_pk_add_f16 v0, v0, v118
	v_pk_add_f16 v100, v100, v119
	v_cvt_pk_f16_f32 v144, v60, v61
	v_cvt_pk_f16_f32 v145, v62, v63
	ds_read_b64_tr_b16 v[60:61], v212 offset:48128
	ds_read_b64_tr_b16 v[62:63], v212 offset:48640
	v_mfma_f32_32x32x16_bf16 v[36:51], v[156:159], v[132:135], v[36:51]
	s_nop 0
	v_pk_add_f16 v0, v0, v144
	v_pk_add_f16 v165, v100, v145
	v_cvt_pk_f16_f32 v146, v64, v65
	v_cvt_pk_f16_f32 v147, v66, v67
	s_add_u32 s14, s14, 0xbf4000
	s_addc_u32 s15, s15, 0
	s_add_i32 s44, s44, 0x12000
	s_mov_b32 m0, s44
	s_nop 0
	global_load_lds_dwordx4 v164, s[14:15]
	s_waitcnt lgkmcnt(14)
	v_mfma_f32_32x32x16_f16 v[4:19], v[124:127], v[160:163], v[4:19]
	v_exp_f32_e32 v68, v68
	v_exp_f32_e32 v69, v69
	v_exp_f32_e32 v70, v70
	v_exp_f32_e32 v71, v71
	s_waitcnt lgkmcnt(12)
	v_mfma_f32_32x32x16_f16 v[20:35], v[124:127], v[84:87], v[20:35]
	v_exp_f32_e32 v72, v72
	v_exp_f32_e32 v73, v73
	v_exp_f32_e32 v74, v74
	v_exp_f32_e32 v75, v75
	ds_read_b128 v[64:67], v210 offset:8192
	ds_read_b128 v[104:107], v210 offset:8704
	s_waitcnt lgkmcnt(12)
	v_mfma_f32_32x32x16_f16 v[4:19], v[120:123], v[88:91], v[4:19]
	v_exp_f32_e32 v76, v76
	v_exp_f32_e32 v77, v77
	v_exp_f32_e32 v78, v78
	v_exp_f32_e32 v79, v79
	ds_read_b128 v[108:111], v210 offset:10240
	ds_read_b128 v[112:115], v210 offset:10752
	s_waitcnt lgkmcnt(12)
	v_mfma_f32_32x32x16_f16 v[20:35], v[120:123], v[92:95], v[20:35]
	v_exp_f32_e32 v80, v80
	v_exp_f32_e32 v81, v81
	v_exp_f32_e32 v82, v82
	v_exp_f32_e32 v83, v83
	ds_read_b128 v[148:151], v210 offset:12288
	ds_read_b128 v[152:155], v210 offset:12800
	s_waitcnt lgkmcnt(12)
	v_mfma_f32_32x32x16_f16 v[4:19], v[116:119], v[96:99], v[4:19]
	v_exp_f32_e32 v36, v36
	v_exp_f32_e32 v37, v37
	v_exp_f32_e32 v38, v38
	v_exp_f32_e32 v39, v39
	ds_read_b128 v[156:159], v210 offset:14336
	ds_read_b128 v[100:103], v210 offset:14848
	s_waitcnt lgkmcnt(12)
	v_mfma_f32_32x32x16_f16 v[20:35], v[116:119], v[52:55], v[20:35]
	v_exp_f32_e32 v40, v40
	v_exp_f32_e32 v41, v41
	v_exp_f32_e32 v42, v42
	v_exp_f32_e32 v43, v43
	s_waitcnt lgkmcnt(10)
	v_mfma_f32_32x32x16_f16 v[4:19], v[144:147], v[56:59], v[4:19]
	v_exp_f32_e32 v44, v44
	v_exp_f32_e32 v45, v45
	v_exp_f32_e32 v46, v46
	v_exp_f32_e32 v47, v47
	s_waitcnt lgkmcnt(8)
	v_mfma_f32_32x32x16_f16 v[20:35], v[144:147], v[60:63], v[20:35]
	v_exp_f32_e32 v48, v48
	v_exp_f32_e32 v49, v49
	v_exp_f32_e32 v50, v50
	v_exp_f32_e32 v51, v51
	s_waitcnt vmcnt(2) lgkmcnt(0)
	s_barrier
	ds_read_b64_tr_b16 v[160:161], v211 offset:49152
	ds_read_b64_tr_b16 v[162:163], v211 offset:49664
	s_waitcnt lgkmcnt(9)
	v_mfma_f32_32x32x16_bf16 v[84:99], v[64:67], v[140:143], -4.0
	v_mov_b32_e32 v116, v3
	v_pk_add_f16 v0, v0, v146
	v_pk_add_f16 v52, v165, v147
	v_cvt_pk_f16_f32 v124, v68, v69
	v_pk_add_f16 v0, v0, v52
	v_cvt_pk_f16_f32 v125, v70, v71
	v_dot2c_f32_f16_e32 v2, 0x3c003c00, v0
	v_mov_b32_e32 v0, v3
	ds_read_b64_tr_b16 v[68:69], v211 offset:53248
	ds_read_b64_tr_b16 v[70:71], v211 offset:53760
	s_waitcnt lgkmcnt(10)
	v_mfma_f32_32x32x16_bf16 v[52:67], v[104:107], v[140:143], -4.0
	s_nop 0
	v_pk_add_f16 v0, v0, v124
	v_pk_add_f16 v104, v116, v125
	v_cvt_pk_f16_f32 v126, v72, v73
	v_cvt_pk_f16_f32 v127, v74, v75
	ds_read_b64_tr_b16 v[72:73], v211 offset:50176
	ds_read_b64_tr_b16 v[74:75], v211 offset:50688
	s_waitcnt lgkmcnt(11)
	v_mfma_f32_32x32x16_bf16 v[84:99], v[108:111], v[128:131], v[84:99]
	v_pk_add_f16 v0, v0, v126
	v_pk_add_f16 v104, v104, v127
	v_cvt_pk_f16_f32 v120, v76, v77
	v_cvt_pk_f16_f32 v121, v78, v79
	ds_read_b64_tr_b16 v[76:77], v211 offset:54272
	ds_read_b64_tr_b16 v[78:79], v211 offset:54784
	s_waitcnt lgkmcnt(12)
	v_mfma_f32_32x32x16_bf16 v[52:67], v[112:115], v[128:131], v[52:67]
	v_pk_add_f16 v0, v0, v120
	v_pk_add_f16 v104, v104, v121
	v_cvt_pk_f16_f32 v122, v80, v81
	v_cvt_pk_f16_f32 v123, v82, v83
	ds_read_b64_tr_b16 v[80:81], v211 offset:51200
	ds_read_b64_tr_b16 v[82:83], v211 offset:51712
	s_waitcnt lgkmcnt(13)
	v_mfma_f32_32x32x16_bf16 v[84:99], v[148:151], v[136:139], v[84:99]
	v_pk_add_f16 v0, v0, v122
	v_pk_add_f16 v104, v104, v123
	v_cvt_pk_f16_f32 v116, v36, v37
	v_cvt_pk_f16_f32 v117, v38, v39
	ds_read_b64_tr_b16 v[36:37], v211 offset:55296
	ds_read_b64_tr_b16 v[38:39], v211 offset:55808
	s_waitcnt lgkmcnt(14)
	v_mfma_f32_32x32x16_bf16 v[52:67], v[152:155], v[136:139], v[52:67]
	v_pk_add_f16 v0, v0, v116
	v_pk_add_f16 v104, v104, v117
	v_cvt_pk_f16_f32 v118, v40, v41
	v_cvt_pk_f16_f32 v119, v42, v43
	ds_read_b64_tr_b16 v[40:41], v211 offset:52224
	ds_read_b64_tr_b16 v[42:43], v211 offset:52736
	s_waitcnt lgkmcnt(14)
	v_mfma_f32_32x32x16_bf16 v[84:99], v[156:159], v[132:135], v[84:99]
	v_pk_add_f16 v0, v0, v118
	v_pk_add_f16 v104, v104, v119
	v_cvt_pk_f16_f32 v144, v44, v45
	v_cvt_pk_f16_f32 v145, v46, v47
	ds_read_b64_tr_b16 v[44:45], v211 offset:56320
	ds_read_b64_tr_b16 v[46:47], v211 offset:56832
	v_mfma_f32_32x32x16_bf16 v[52:67], v[100:103], v[132:135], v[52:67]
	v_pk_add_f16 v0, v0, v144
	v_pk_add_f16 v164, v104, v145
	v_cvt_pk_f16_f32 v146, v48, v49
	v_cvt_pk_f16_f32 v147, v50, v51
	s_waitcnt lgkmcnt(14)
	v_mfma_f32_32x32x16_f16 v[4:19], v[124:127], v[160:163], v[4:19]
	v_exp_f32_e32 v84, v84
	v_exp_f32_e32 v85, v85
	v_exp_f32_e32 v86, v86
	v_exp_f32_e32 v87, v87
	s_waitcnt lgkmcnt(12)
	v_mfma_f32_32x32x16_f16 v[20:35], v[124:127], v[68:71], v[20:35]
	v_exp_f32_e32 v88, v88
	v_exp_f32_e32 v89, v89
	v_exp_f32_e32 v90, v90
	v_exp_f32_e32 v91, v91
	ds_read_b128 v[48:51], v210 offset:16384
	ds_read_b128 v[100:103], v210 offset:16896
	s_waitcnt lgkmcnt(12)
	v_mfma_f32_32x32x16_f16 v[4:19], v[120:123], v[72:75], v[4:19]
	v_exp_f32_e32 v92, v92
	v_exp_f32_e32 v93, v93
	v_exp_f32_e32 v94, v94
	v_exp_f32_e32 v95, v95
	ds_read_b128 v[104:107], v210 offset:18432
	ds_read_b128 v[108:111], v210 offset:18944
	s_waitcnt lgkmcnt(12)
	v_mfma_f32_32x32x16_f16 v[20:35], v[120:123], v[76:79], v[20:35]
	v_exp_f32_e32 v96, v96
	v_exp_f32_e32 v97, v97
	v_exp_f32_e32 v98, v98
	v_exp_f32_e32 v99, v99
	ds_read_b128 v[112:115], v210 offset:20480
	ds_read_b128 v[148:151], v210 offset:20992
	s_waitcnt lgkmcnt(12)
	v_mfma_f32_32x32x16_f16 v[4:19], v[116:119], v[80:83], v[4:19]
	v_exp_f32_e32 v52, v52
	v_exp_f32_e32 v53, v53
	v_exp_f32_e32 v54, v54
	v_exp_f32_e32 v55, v55
	ds_read_b128 v[152:155], v210 offset:22528
	ds_read_b128 v[156:159], v210 offset:23040
	s_waitcnt lgkmcnt(12)
	v_mfma_f32_32x32x16_f16 v[20:35], v[116:119], v[36:39], v[20:35]
	v_exp_f32_e32 v56, v56
	v_exp_f32_e32 v57, v57
	v_exp_f32_e32 v58, v58
	v_exp_f32_e32 v59, v59
	s_waitcnt lgkmcnt(10)
	v_mfma_f32_32x32x16_f16 v[4:19], v[144:147], v[40:43], v[4:19]
	v_exp_f32_e32 v60, v60
	v_exp_f32_e32 v61, v61
	v_exp_f32_e32 v62, v62
	v_exp_f32_e32 v63, v63
	s_waitcnt lgkmcnt(8)
	v_mfma_f32_32x32x16_f16 v[20:35], v[144:147], v[44:47], v[20:35]
	v_exp_f32_e32 v64, v64
	v_exp_f32_e32 v65, v65
	v_exp_f32_e32 v66, v66
	v_exp_f32_e32 v67, v67
	ds_read_b64_tr_b16 v[160:161], v211 offset:57344
	ds_read_b64_tr_b16 v[162:163], v211 offset:57856
	s_waitcnt lgkmcnt(9)
	v_mfma_f32_32x32x16_bf16 v[68:83], v[48:51], v[140:143], -4.0
	v_cvt_pk_f16_f32 v124, v84, v85
	v_pk_add_f16 v0, v0, v146
	v_pk_add_f16 v116, v164, v147
	v_cvt_pk_f16_f32 v125, v86, v87
	ds_read_b64_tr_b16 v[84:85], v211 offset:61440
	ds_read_b64_tr_b16 v[86:87], v211 offset:61952
	s_waitcnt lgkmcnt(10)
	v_mfma_f32_32x32x16_bf16 v[36:51], v[100:103], v[140:143], -4.0
	s_nop 0
	v_pk_add_f16 v0, v0, v124
	v_pk_add_f16 v100, v116, v125
	v_cvt_pk_f16_f32 v126, v88, v89
	v_cvt_pk_f16_f32 v127, v90, v91
	ds_read_b64_tr_b16 v[88:89], v211 offset:58368
	ds_read_b64_tr_b16 v[90:91], v211 offset:58880
	s_waitcnt lgkmcnt(11)
	v_mfma_f32_32x32x16_bf16 v[68:83], v[104:107], v[128:131], v[68:83]
	v_pk_add_f16 v0, v0, v126
	v_pk_add_f16 v100, v100, v127
	v_cvt_pk_f16_f32 v120, v92, v93
	v_cvt_pk_f16_f32 v121, v94, v95
	ds_read_b64_tr_b16 v[92:93], v211 offset:62464
	ds_read_b64_tr_b16 v[94:95], v211 offset:62976
	s_waitcnt lgkmcnt(12)
	v_mfma_f32_32x32x16_bf16 v[36:51], v[108:111], v[128:131], v[36:51]
	s_nop 0
	v_pk_add_f16 v0, v0, v120
	v_pk_add_f16 v100, v100, v121
	v_cvt_pk_f16_f32 v122, v96, v97
	v_cvt_pk_f16_f32 v123, v98, v99
	ds_read_b64_tr_b16 v[96:97], v211 offset:59392
	ds_read_b64_tr_b16 v[98:99], v211 offset:59904
	s_waitcnt lgkmcnt(13)
	v_mfma_f32_32x32x16_bf16 v[68:83], v[112:115], v[136:139], v[68:83]
	v_pk_add_f16 v0, v0, v122
	v_pk_add_f16 v100, v100, v123
	v_cvt_pk_f16_f32 v116, v52, v53
	v_cvt_pk_f16_f32 v117, v54, v55
	ds_read_b64_tr_b16 v[52:53], v211 offset:63488
	ds_read_b64_tr_b16 v[54:55], v211 offset:64000
	s_waitcnt lgkmcnt(14)
	v_mfma_f32_32x32x16_bf16 v[36:51], v[148:151], v[136:139], v[36:51]
	s_nop 0
	v_pk_add_f16 v0, v0, v116
	v_pk_add_f16 v100, v100, v117
	v_cvt_pk_f16_f32 v118, v56, v57
	v_cvt_pk_f16_f32 v119, v58, v59
	ds_read_b64_tr_b16 v[56:57], v211 offset:60416
	ds_read_b64_tr_b16 v[58:59], v211 offset:60928
	s_waitcnt lgkmcnt(14)
	v_mfma_f32_32x32x16_bf16 v[68:83], v[152:155], v[132:135], v[68:83]
	v_pk_add_f16 v0, v0, v118
	v_pk_add_f16 v100, v100, v119
	v_cvt_pk_f16_f32 v144, v60, v61
	v_cvt_pk_f16_f32 v145, v62, v63
	ds_read_b64_tr_b16 v[60:61], v211 offset:64512
	ds_read_b64_tr_b16 v[62:63], v211 offset:65024
	v_mfma_f32_32x32x16_bf16 v[36:51], v[156:159], v[132:135], v[36:51]
	s_nop 0
	v_pk_add_f16 v0, v0, v144
	v_pk_add_f16 v164, v100, v145
	v_cvt_pk_f16_f32 v146, v64, v65
	v_cvt_pk_f16_f32 v147, v66, v67
	s_waitcnt lgkmcnt(14)
	v_mfma_f32_32x32x16_f16 v[4:19], v[124:127], v[160:163], v[4:19]
	v_exp_f32_e32 v68, v68
	v_exp_f32_e32 v69, v69
	v_exp_f32_e32 v70, v70
	v_exp_f32_e32 v71, v71
	s_waitcnt lgkmcnt(12)
	v_mfma_f32_32x32x16_f16 v[20:35], v[124:127], v[84:87], v[20:35]
	v_exp_f32_e32 v72, v72
	v_exp_f32_e32 v73, v73
	v_exp_f32_e32 v74, v74
	v_exp_f32_e32 v75, v75
	ds_read_b128 v[84:87], v210 offset:24576
	ds_read_b128 v[104:107], v210 offset:25088
	s_waitcnt lgkmcnt(12)
	v_mfma_f32_32x32x16_f16 v[4:19], v[120:123], v[88:91], v[4:19]
	v_exp_f32_e32 v76, v76
	v_exp_f32_e32 v77, v77
	v_exp_f32_e32 v78, v78
	v_exp_f32_e32 v79, v79
	ds_read_b128 v[108:111], v210 offset:26624
	ds_read_b128 v[112:115], v210 offset:27136
	s_waitcnt lgkmcnt(12)
	v_mfma_f32_32x32x16_f16 v[20:35], v[120:123], v[92:95], v[20:35]
	v_exp_f32_e32 v80, v80
	v_exp_f32_e32 v81, v81
	v_exp_f32_e32 v82, v82
	v_exp_f32_e32 v83, v83
	ds_read_b128 v[148:151], v210 offset:28672
	ds_read_b128 v[152:155], v210 offset:29184
	s_waitcnt lgkmcnt(12)
	v_mfma_f32_32x32x16_f16 v[4:19], v[116:119], v[96:99], v[4:19]
	v_exp_f32_e32 v36, v36
	v_exp_f32_e32 v37, v37
	v_exp_f32_e32 v38, v38
	v_exp_f32_e32 v39, v39
	ds_read_b128 v[156:159], v210 offset:30720
	ds_read_b128 v[160:163], v210 offset:31232
	s_waitcnt lgkmcnt(12)
	v_mfma_f32_32x32x16_f16 v[20:35], v[116:119], v[52:55], v[20:35]
	v_exp_f32_e32 v40, v40
	v_exp_f32_e32 v41, v41
	v_exp_f32_e32 v42, v42
	v_exp_f32_e32 v43, v43
	s_waitcnt lgkmcnt(10)
	v_mfma_f32_32x32x16_f16 v[4:19], v[144:147], v[56:59], v[4:19]
	v_exp_f32_e32 v44, v44
	v_exp_f32_e32 v45, v45
	v_exp_f32_e32 v46, v46
	v_exp_f32_e32 v47, v47
	s_waitcnt lgkmcnt(8)
	v_mfma_f32_32x32x16_f16 v[20:35], v[144:147], v[60:63], v[20:35]
	v_exp_f32_e32 v48, v48
	v_exp_f32_e32 v49, v49
	v_exp_f32_e32 v50, v50
	v_exp_f32_e32 v51, v51
	s_waitcnt vmcnt(0) lgkmcnt(0)
	s_barrier
	ds_read_b64_tr_b16 v[100:101], v212 offset:16384
	ds_read_b64_tr_b16 v[102:103], v212 offset:16896
	s_waitcnt lgkmcnt(9)
	v_mfma_f32_32x32x16_bf16 v[52:67], v[84:87], v[140:143], -4.0
	v_mov_b32_e32 v116, v3
	v_pk_add_f16 v0, v0, v146
	v_pk_add_f16 v84, v164, v147
	v_cvt_pk_f16_f32 v124, v68, v69
	v_pk_add_f16 v0, v0, v84
	v_cvt_pk_f16_f32 v125, v70, v71
	v_dot2c_f32_f16_e32 v2, 0x3c003c00, v0
	v_mov_b32_e32 v0, v3
	ds_read_b64_tr_b16 v[68:69], v212 offset:20480
	ds_read_b64_tr_b16 v[70:71], v212 offset:20992
	s_waitcnt lgkmcnt(10)
	v_mfma_f32_32x32x16_bf16 v[84:99], v[104:107], v[140:143], -4.0
	s_nop 0
	v_pk_add_f16 v0, v0, v124
	v_pk_add_f16 v104, v116, v125
	v_cvt_pk_f16_f32 v126, v72, v73
	v_cvt_pk_f16_f32 v127, v74, v75
	ds_read_b64_tr_b16 v[72:73], v212 offset:17408
	ds_read_b64_tr_b16 v[74:75], v212 offset:17920
	s_waitcnt lgkmcnt(11)
	v_mfma_f32_32x32x16_bf16 v[52:67], v[108:111], v[128:131], v[52:67]
	v_pk_add_f16 v0, v0, v126
	v_pk_add_f16 v104, v104, v127
	v_cvt_pk_f16_f32 v120, v76, v77
	v_cvt_pk_f16_f32 v121, v78, v79
	ds_read_b64_tr_b16 v[76:77], v212 offset:21504
	ds_read_b64_tr_b16 v[78:79], v212 offset:22016
	s_waitcnt lgkmcnt(12)
	v_mfma_f32_32x32x16_bf16 v[84:99], v[112:115], v[128:131], v[84:99]
	v_pk_add_f16 v0, v0, v120
	v_pk_add_f16 v104, v104, v121
	v_cvt_pk_f16_f32 v122, v80, v81
	v_cvt_pk_f16_f32 v123, v82, v83
	ds_read_b64_tr_b16 v[80:81], v212 offset:18432
	ds_read_b64_tr_b16 v[82:83], v212 offset:18944
	s_waitcnt lgkmcnt(13)
	v_mfma_f32_32x32x16_bf16 v[52:67], v[148:151], v[136:139], v[52:67]
	v_pk_add_f16 v0, v0, v122
	v_pk_add_f16 v104, v104, v123
	v_cvt_pk_f16_f32 v116, v36, v37
	v_cvt_pk_f16_f32 v117, v38, v39
	ds_read_b64_tr_b16 v[36:37], v212 offset:22528
	ds_read_b64_tr_b16 v[38:39], v212 offset:23040
	s_waitcnt lgkmcnt(14)
	v_mfma_f32_32x32x16_bf16 v[84:99], v[152:155], v[136:139], v[84:99]
	v_pk_add_f16 v0, v0, v116
	v_pk_add_f16 v104, v104, v117
	v_cvt_pk_f16_f32 v118, v40, v41
	v_cvt_pk_f16_f32 v119, v42, v43
	ds_read_b64_tr_b16 v[40:41], v212 offset:19456
	ds_read_b64_tr_b16 v[42:43], v212 offset:19968
	s_waitcnt lgkmcnt(14)
	v_mfma_f32_32x32x16_bf16 v[52:67], v[156:159], v[132:135], v[52:67]
	v_pk_add_f16 v0, v0, v118
	v_pk_add_f16 v104, v104, v119
	v_cvt_pk_f16_f32 v144, v44, v45
	v_cvt_pk_f16_f32 v145, v46, v47
	ds_read_b64_tr_b16 v[44:45], v212 offset:23552
	ds_read_b64_tr_b16 v[46:47], v212 offset:24064
	v_mfma_f32_32x32x16_bf16 v[84:99], v[160:163], v[132:135], v[84:99]
	v_pk_add_f16 v0, v0, v144
	v_pk_add_f16 v104, v104, v145
	v_cvt_pk_f16_f32 v146, v48, v49
	v_cvt_pk_f16_f32 v147, v50, v51
	s_nop 0
	v_exp_f32_e32 v52, v52
	v_exp_f32_e32 v53, v53
	v_exp_f32_e32 v54, v54
	v_exp_f32_e32 v55, v55
	s_nop 0
	v_exp_f32_e32 v56, v56
	v_exp_f32_e32 v57, v57
	v_exp_f32_e32 v58, v58
	v_exp_f32_e32 v59, v59
	s_nop 0
	v_exp_f32_e32 v60, v60
	v_exp_f32_e32 v61, v61
	v_exp_f32_e32 v62, v62
	v_exp_f32_e32 v63, v63
	s_nop 0
	v_exp_f32_e32 v64, v64
	v_exp_f32_e32 v65, v65
	v_exp_f32_e32 v66, v66
	v_exp_f32_e32 v67, v67
	v_exp_f32_e32 v84, v84
	v_exp_f32_e32 v85, v85
	v_exp_f32_e32 v86, v86
	v_exp_f32_e32 v87, v87
	s_nop 0
	v_exp_f32_e32 v88, v88
	v_exp_f32_e32 v89, v89
	v_exp_f32_e32 v90, v90
	v_exp_f32_e32 v91, v91
	s_nop 0
	v_exp_f32_e32 v92, v92
	v_exp_f32_e32 v93, v93
	v_exp_f32_e32 v94, v94
	v_exp_f32_e32 v95, v95
	s_nop 0
	v_exp_f32_e32 v96, v96
	v_exp_f32_e32 v97, v97
	v_exp_f32_e32 v98, v98
	v_exp_f32_e32 v99, v99
	s_waitcnt lgkmcnt(14)
	v_mfma_f32_32x32x16_f16 v[4:19], v[124:127], v[100:103], v[4:19]
	v_pk_add_f16 v0, v0, v146
	v_cvt_pk_f16_f32 v48, v52, v53
	v_cvt_pk_f16_f32 v52, v60, v61
	v_cvt_pk_f16_f32 v49, v54, v55
	v_cvt_pk_f16_f32 v50, v56, v57
	v_cvt_pk_f16_f32 v54, v64, v65
	v_cvt_pk_f16_f32 v56, v84, v85
	s_waitcnt lgkmcnt(12)
	v_mfma_f32_32x32x16_f16 v[20:35], v[124:127], v[68:71], v[20:35]
	v_pk_add_f16 v68, v104, v147
	v_cvt_pk_f16_f32 v60, v92, v93
	v_pk_add_f16 v0, v0, v48
	v_pk_add_f16 v64, v68, v52
	v_cvt_pk_f16_f32 v53, v62, v63
	v_pk_add_f16 v0, v0, v56
	v_pk_add_f16 v64, v64, v60
	s_waitcnt lgkmcnt(10)
	v_mfma_f32_32x32x16_f16 v[4:19], v[120:123], v[72:75], v[4:19]
	v_cvt_pk_f16_f32 v57, v86, v87
	v_cvt_pk_f16_f32 v61, v94, v95
	v_pk_add_f16 v0, v0, v49
	v_cvt_pk_f16_f32 v51, v58, v59
	v_pk_add_f16 v0, v0, v57
	v_cvt_pk_f16_f32 v58, v88, v89
	v_cvt_pk_f16_f32 v62, v96, v97
	s_waitcnt lgkmcnt(8)
	v_mfma_f32_32x32x16_f16 v[20:35], v[120:123], v[76:79], v[20:35]
	v_pk_add_f16 v0, v0, v50
	v_cvt_pk_f16_f32 v55, v66, v67
	v_pk_add_f16 v0, v0, v58
	v_cvt_pk_f16_f32 v59, v90, v91
	v_cvt_pk_f16_f32 v63, v98, v99
	v_pk_add_f16 v0, v0, v51
	s_waitcnt lgkmcnt(6)
	v_mfma_f32_32x32x16_f16 v[4:19], v[116:119], v[80:83], v[4:19]
	v_pk_add_f16 v0, v0, v59
	s_waitcnt lgkmcnt(4)
	v_mfma_f32_32x32x16_f16 v[20:35], v[116:119], v[36:39], v[20:35]
	v_pk_add_f16 v36, v64, v53
	s_nop 0
	v_pk_add_f16 v36, v36, v61
	s_nop 0
	v_pk_add_f16 v36, v36, v54
	s_nop 0
	v_pk_add_f16 v36, v36, v62
	s_waitcnt lgkmcnt(2)
	v_mfma_f32_32x32x16_f16 v[4:19], v[144:147], v[40:43], v[4:19]
	v_pk_add_f16 v36, v36, v55
	s_nop 0
	v_pk_add_f16 v36, v36, v63
	s_nop 0
	v_pk_add_f16 v0, v36, v0
	s_nop 0
	v_dot2c_f32_f16_e32 v2, 0x3c003c00, v0
	s_waitcnt lgkmcnt(0)
	v_mfma_f32_32x32x16_f16 v[20:35], v[144:147], v[44:47], v[20:35]
	ds_read_b64_tr_b16 v[36:37],v214 offset:0
	ds_read_b64_tr_b16 v[38:39],v214 offset:512
	ds_read_b64_tr_b16 v[40:41],v214 offset:1024
	ds_read_b64_tr_b16 v[42:43],v214 offset:1536
	ds_read_b64_tr_b16 v[44:45],v214 offset:2048
	ds_read_b64_tr_b16 v[46:47],v214 offset:2560
	ds_read_b64_tr_b16 v[64:65],v214 offset:3072
	ds_read_b64_tr_b16 v[66:67],v214 offset:3584
	s_waitcnt lgkmcnt(0)
	s_nop 0
	v_mfma_f32_32x32x16_f16 v[4:19], v[48:51], v[36:39], v[4:19]
	ds_read_b64_tr_b16 v[36:37],v214 offset:4096
	ds_read_b64_tr_b16 v[38:39],v214 offset:4608
	v_mfma_f32_32x32x16_f16 v[4:19], v[52:55], v[40:43], v[4:19]
	ds_read_b64_tr_b16 v[40:41],v214 offset:5120
	ds_read_b64_tr_b16 v[42:43],v214 offset:5632
	v_mfma_f32_32x32x16_f16 v[4:19], v[56:59], v[44:47], v[4:19]
	ds_read_b64_tr_b16 v[44:45],v214 offset:6144
	ds_read_b64_tr_b16 v[46:47],v214 offset:6656
	v_mfma_f32_32x32x16_f16 v[4:19], v[60:63], v[64:67], v[4:19]
	ds_read_b64_tr_b16 v[64:65],v214 offset:7168
	ds_read_b64_tr_b16 v[66:67],v214 offset:7680
	s_waitcnt lgkmcnt(0)
	v_mfma_f32_32x32x16_f16 v[20:35], v[48:51], v[36:39], v[20:35]
	v_mov_b32_e32 v36, v2
	s_nop 1
	v_permlane32_swap_b32_e32 v2, v36
	v_mfma_f32_32x32x16_f16 v[20:35], v[52:55], v[40:43], v[20:35]
	v_mfma_f32_32x32x16_f16 v[20:35], v[56:59], v[44:47], v[20:35]
	v_mfma_f32_32x32x16_f16 v[20:35], v[60:63], v[64:67], v[20:35]
	s_and_saveexec_b64 s[14:15], s[4:5]
	s_cbranch_execz .LBB0_241
	v_add_f32_e32 v0, v2, v36
	v_lshl_add_u32 v2, v207, 2, s11
	ds_write_b32 v2, v0 offset:128
	s_branch .LBB0_241
